# bf16 GEMM K-loops: ds_read fragment loads first in every load block (LDS constants as literals), SALU address math and LDS-DMA issue behind them
# speedup vs baseline: 1.0040x; 1.0001x over previous
.LBB0_847:
	v_add_u32_e32 v84, 0x10000, v231
	v_add_u32_e32 v128, 0x14000, v231
	ds_read_b128 v[68:71], v84
	ds_read_b128 v[72:75], v84 offset:1024
	ds_read_b128 v[76:79], v84 offset:2048
	ds_read_b128 v[84:87], v84 offset:3072
	ds_read_b128 v[92:95], v128
	ds_read_b128 v[100:103], v128 offset:1024
	ds_read_b128 v[116:119], v128 offset:2048
	ds_read_b128 v[128:131], v128 offset:3072
	ds_read_b128 v[140:143], v232
	ds_read_b128 v[152:155], v232 offset:1024
	ds_read_b128 v[164:167], v232 offset:2048
	ds_read_b128 v[172:175], v232 offset:3072
	ds_read_b128 v[180:183], v232 offset:4096
	ds_read_b128 v[184:187], v232 offset:5120
	ds_read_b128 v[188:191], v232 offset:6144
	ds_read_b128 v[192:195], v232 offset:7168
	s_add_u32 s15, s38, 0xfffc0080
	s_addc_u32 s17, s39, -1
	s_cmp_eq_u32 s3, 12
	s_cselect_b64 s[26:27], -1, 0
	s_and_b64 s[34:35], s[26:27], exec
	s_cselect_b32 s17, 0, s17
	s_cselect_b32 s15, 0, s15
	s_and_b64 s[26:27], s[26:27], s[36:37]
	s_and_b64 s[34:35], s[26:27], exec
	s_cselect_b32 s28, s20, s30
	s_cselect_b32 s23, s21, s31
	s_add_u32 s42, s28, s15
	s_addc_u32 s43, s23, s17
	s_add_i32 s23, 0, 0x10000
	s_and_b64 s[26:27], s[26:27], exec
	s_cselect_b32 s28, s19, s1
	s_cselect_b32 s33, s18, s0
	s_add_i32 s34, 0, 0x14000
	s_add_i32 m0, s55, 0xc000
	s_add_u32 s26, s0, s38
	s_addc_u32 s27, s1, s39
	global_load_lds_dwordx4 v2, s[26:27]
	s_add_i32 m0, s55, 0xe000
	v_mov_b32_e32 v219, v3
	global_load_lds_dwordx4 v218, s[26:27]
	s_waitcnt vmcnt(8)
	s_waitcnt lgkmcnt(0)
	s_barrier
	s_setprio 1
	s_waitcnt lgkmcnt(0)
	v_mfma_f32_16x16x32_bf16 v[176:179], v[68:71], v[140:143], v[176:179]
	v_mfma_f32_16x16x32_bf16 v[168:171], v[76:79], v[140:143], v[168:171]
	v_mfma_f32_16x16x32_bf16 v[148:151], v[68:71], v[164:167], v[148:151]
	v_mfma_f32_16x16x32_bf16 v[144:147], v[76:79], v[164:167], v[144:147]
	v_mfma_f32_16x16x32_bf16 v[124:127], v[68:71], v[180:183], v[124:127]
	v_mfma_f32_16x16x32_bf16 v[120:123], v[76:79], v[180:183], v[120:123]
	v_mfma_f32_16x16x32_bf16 v[104:107], v[68:71], v[188:191], v[104:107]
	v_mfma_f32_16x16x32_bf16 v[96:99], v[76:79], v[188:191], v[96:99]
	v_mfma_f32_16x16x32_bf16 v[176:179], v[72:75], v[152:155], v[176:179]
	v_mfma_f32_16x16x32_bf16 v[168:171], v[84:87], v[152:155], v[168:171]
	v_mfma_f32_16x16x32_bf16 v[148:151], v[72:75], v[172:175], v[148:151]
	v_mfma_f32_16x16x32_bf16 v[144:147], v[84:87], v[172:175], v[144:147]
	v_mfma_f32_16x16x32_bf16 v[124:127], v[72:75], v[184:187], v[124:127]
	v_mfma_f32_16x16x32_bf16 v[120:123], v[84:87], v[184:187], v[120:123]
	v_mfma_f32_16x16x32_bf16 v[104:107], v[72:75], v[192:195], v[104:107]
	v_mfma_f32_16x16x32_bf16 v[96:99], v[84:87], v[192:195], v[96:99]
	s_setprio 0
	s_setprio 1
	v_mfma_f32_16x16x32_bf16 v[160:163], v[92:95], v[140:143], v[160:163]
	v_mfma_f32_16x16x32_bf16 v[136:139], v[92:95], v[164:167], v[136:139]
	v_mfma_f32_16x16x32_bf16 v[132:135], v[116:119], v[164:167], v[132:135]
	v_mfma_f32_16x16x32_bf16 v[112:115], v[92:95], v[180:183], v[112:115]
	v_mfma_f32_16x16x32_bf16 v[108:111], v[116:119], v[180:183], v[108:111]
	v_mfma_f32_16x16x32_bf16 v[88:91], v[92:95], v[188:191], v[88:91]
	v_mfma_f32_16x16x32_bf16 v[80:83], v[116:119], v[188:191], v[80:83]
	v_mfma_f32_16x16x32_bf16 v[160:163], v[100:103], v[152:155], v[160:163]
	v_mfma_f32_16x16x32_bf16 v[140:143], v[116:119], v[140:143], v[156:159]
	v_mfma_f32_16x16x32_bf16 v[136:139], v[100:103], v[172:175], v[136:139]
	v_mfma_f32_16x16x32_bf16 v[132:135], v[128:131], v[172:175], v[132:135]
	v_mfma_f32_16x16x32_bf16 v[112:115], v[100:103], v[184:187], v[112:115]
	v_mfma_f32_16x16x32_bf16 v[108:111], v[128:131], v[184:187], v[108:111]
	v_mfma_f32_16x16x32_bf16 v[88:91], v[100:103], v[192:195], v[88:91]
	v_mfma_f32_16x16x32_bf16 v[80:83], v[128:131], v[192:195], v[80:83]
	v_mfma_f32_16x16x32_bf16 v[140:143], v[128:131], v[152:155], v[140:143]
	s_setprio 0
	s_barrier
	ds_read_b128 v[152:155], v232 offset:16384
	ds_read_b128 v[156:159], v232 offset:17408
	ds_read_b128 v[164:167], v232 offset:18432
	ds_read_b128 v[172:175], v232 offset:19456
	ds_read_b128 v[180:183], v232 offset:20480
	ds_read_b128 v[184:187], v232 offset:21504
	ds_read_b128 v[188:191], v232 offset:22528
	ds_read_b128 v[192:195], v232 offset:23552
	s_add_i32 s23, s23, s54
	s_mov_b32 m0, s23
	global_load_lds_dwordx4 v216, s[42:43]
	s_add_i32 m0, s23, 0x2000
	s_add_u32 s26, s42, 0x40000
	s_addc_u32 s27, s43, 0
	s_add_i32 s23, s34, s54
	global_load_lds_dwordx4 v220, s[42:43]
	s_mov_b32 m0, s23
	v_mov_b32_e32 v217, v3
	global_load_lds_dwordx4 v216, s[26:27]
	s_add_i32 m0, s23, 0x2000
	v_mov_b32_e32 v221, v3
	global_load_lds_dwordx4 v220, s[26:27]
	s_add_u32 s26, s33, s15
	s_addc_u32 s27, s28, s17
	s_mov_b32 m0, s55
	v_lshl_add_u64 v[196:197], s[42:43], 0, v[216:217]
	global_load_lds_dwordx4 v2, s[26:27]
	s_mov_b32 m0, s56
	v_lshl_add_u64 v[198:199], s[42:43], 0, v[220:221]
	global_load_lds_dwordx4 v218, s[26:27]
	s_waitcnt vmcnt(8)
	s_waitcnt lgkmcnt(0)
	v_lshl_add_u64 v[200:201], s[26:27], 0, v[2:3]
	v_lshl_add_u64 v[202:203], s[26:27], 0, v[218:219]
	s_barrier
	s_setprio 1
	s_waitcnt lgkmcnt(0)
	v_mfma_f32_16x16x32_bf16 v[64:67], v[68:71], v[152:155], v[64:67]
	v_mfma_f32_16x16x32_bf16 v[60:63], v[76:79], v[152:155], v[60:63]
	v_mfma_f32_16x16x32_bf16 v[48:51], v[68:71], v[164:167], v[48:51]
	v_mfma_f32_16x16x32_bf16 v[44:47], v[76:79], v[164:167], v[44:47]
	v_mfma_f32_16x16x32_bf16 v[32:35], v[68:71], v[180:183], v[32:35]
	v_mfma_f32_16x16x32_bf16 v[28:31], v[76:79], v[180:183], v[28:31]
	v_mfma_f32_16x16x32_bf16 v[16:19], v[68:71], v[188:191], v[16:19]
	v_mfma_f32_16x16x32_bf16 v[12:15], v[76:79], v[188:191], v[12:15]
	v_mfma_f32_16x16x32_bf16 v[64:67], v[72:75], v[156:159], v[64:67]
	v_mfma_f32_16x16x32_bf16 v[60:63], v[84:87], v[156:159], v[60:63]
	v_mfma_f32_16x16x32_bf16 v[48:51], v[72:75], v[172:175], v[48:51]
	v_mfma_f32_16x16x32_bf16 v[44:47], v[84:87], v[172:175], v[44:47]
	v_mfma_f32_16x16x32_bf16 v[32:35], v[72:75], v[184:187], v[32:35]
	v_mfma_f32_16x16x32_bf16 v[28:31], v[84:87], v[184:187], v[28:31]
	v_mfma_f32_16x16x32_bf16 v[16:19], v[72:75], v[192:195], v[16:19]
	v_mfma_f32_16x16x32_bf16 v[12:15], v[84:87], v[192:195], v[12:15]
	s_setprio 0
	s_setprio 1
	v_mfma_f32_16x16x32_bf16 v[56:59], v[92:95], v[152:155], v[56:59]
	v_mfma_f32_16x16x32_bf16 v[52:55], v[116:119], v[152:155], v[52:55]
	v_mfma_f32_16x16x32_bf16 v[40:43], v[92:95], v[164:167], v[40:43]
	v_mfma_f32_16x16x32_bf16 v[36:39], v[116:119], v[164:167], v[36:39]
	v_mfma_f32_16x16x32_bf16 v[24:27], v[92:95], v[180:183], v[24:27]
	v_mfma_f32_16x16x32_bf16 v[20:23], v[116:119], v[180:183], v[20:23]
	v_mfma_f32_16x16x32_bf16 v[8:11], v[92:95], v[188:191], v[8:11]
	v_mfma_f32_16x16x32_bf16 v[4:7], v[116:119], v[188:191], v[4:7]
	v_mfma_f32_16x16x32_bf16 v[56:59], v[100:103], v[156:159], v[56:59]
	v_mfma_f32_16x16x32_bf16 v[52:55], v[128:131], v[156:159], v[52:55]
	v_mfma_f32_16x16x32_bf16 v[40:43], v[100:103], v[172:175], v[40:43]
	v_mfma_f32_16x16x32_bf16 v[36:39], v[128:131], v[172:175], v[36:39]
	v_mfma_f32_16x16x32_bf16 v[24:27], v[100:103], v[184:187], v[24:27]
	v_mfma_f32_16x16x32_bf16 v[20:23], v[128:131], v[184:187], v[20:23]
	v_mfma_f32_16x16x32_bf16 v[8:11], v[100:103], v[192:195], v[8:11]
	v_mfma_f32_16x16x32_bf16 v[4:7], v[128:131], v[192:195], v[4:7]
	s_setprio 0
	s_barrier
	v_add_u32_e32 v84, 0x18000, v231
	v_add_u32_e32 v128, 0x1c000, v231
	ds_read_b128 v[68:71], v84
	ds_read_b128 v[72:75], v84 offset:1024
	ds_read_b128 v[76:79], v84 offset:2048
	ds_read_b128 v[84:87], v84 offset:3072
	ds_read_b128 v[92:95], v128
	ds_read_b128 v[100:103], v128 offset:1024
	ds_read_b128 v[116:119], v128 offset:2048
	ds_read_b128 v[128:131], v128 offset:3072
	ds_read_b128 v[152:155], v232 offset:32768
	ds_read_b128 v[156:159], v232 offset:33792
	ds_read_b128 v[164:167], v232 offset:34816
	ds_read_b128 v[172:175], v232 offset:35840
	ds_read_b128 v[180:183], v232 offset:36864
	ds_read_b128 v[184:187], v232 offset:37888
	ds_read_b128 v[188:191], v232 offset:38912
	ds_read_b128 v[192:195], v232 offset:39936
	s_add_i32 s15, 0, 0x18000
	s_add_i32 s17, 0, 0x1c000
	s_add_u32 s26, s26, 0x40000
	s_addc_u32 s27, s27, 0
	s_mov_b32 m0, s57
	global_load_lds_dwordx4 v2, s[26:27]
	s_mov_b32 m0, s58
	s_nop 0
	global_load_lds_dwordx4 v218, s[26:27]
	s_waitcnt vmcnt(8)
	s_waitcnt lgkmcnt(0)
	s_barrier
	s_setprio 1
	s_waitcnt lgkmcnt(0)
	v_mfma_f32_16x16x32_bf16 v[176:179], v[68:71], v[152:155], v[176:179]
	v_mfma_f32_16x16x32_bf16 v[168:171], v[76:79], v[152:155], v[168:171]
	v_mfma_f32_16x16x32_bf16 v[148:151], v[68:71], v[164:167], v[148:151]
	v_mfma_f32_16x16x32_bf16 v[144:147], v[76:79], v[164:167], v[144:147]
	v_mfma_f32_16x16x32_bf16 v[124:127], v[68:71], v[180:183], v[124:127]
	v_mfma_f32_16x16x32_bf16 v[120:123], v[76:79], v[180:183], v[120:123]
	v_mfma_f32_16x16x32_bf16 v[104:107], v[68:71], v[188:191], v[104:107]
	v_mfma_f32_16x16x32_bf16 v[96:99], v[76:79], v[188:191], v[96:99]
	v_mfma_f32_16x16x32_bf16 v[176:179], v[72:75], v[156:159], v[176:179]
	v_mfma_f32_16x16x32_bf16 v[168:171], v[84:87], v[156:159], v[168:171]
	v_mfma_f32_16x16x32_bf16 v[148:151], v[72:75], v[172:175], v[148:151]
	v_mfma_f32_16x16x32_bf16 v[144:147], v[84:87], v[172:175], v[144:147]
	v_mfma_f32_16x16x32_bf16 v[124:127], v[72:75], v[184:187], v[124:127]
	v_mfma_f32_16x16x32_bf16 v[120:123], v[84:87], v[184:187], v[120:123]
	v_mfma_f32_16x16x32_bf16 v[104:107], v[72:75], v[192:195], v[104:107]
	v_mfma_f32_16x16x32_bf16 v[96:99], v[84:87], v[192:195], v[96:99]
	s_setprio 0
	s_setprio 1
	v_mfma_f32_16x16x32_bf16 v[160:163], v[92:95], v[152:155], v[160:163]
	v_mfma_f32_16x16x32_bf16 v[140:143], v[116:119], v[152:155], v[140:143]
	v_mfma_f32_16x16x32_bf16 v[136:139], v[92:95], v[164:167], v[136:139]
	v_mfma_f32_16x16x32_bf16 v[132:135], v[116:119], v[164:167], v[132:135]
	v_mfma_f32_16x16x32_bf16 v[112:115], v[92:95], v[180:183], v[112:115]
	v_mfma_f32_16x16x32_bf16 v[108:111], v[116:119], v[180:183], v[108:111]
	v_mfma_f32_16x16x32_bf16 v[88:91], v[92:95], v[188:191], v[88:91]
	v_mfma_f32_16x16x32_bf16 v[80:83], v[116:119], v[188:191], v[80:83]
	v_mfma_f32_16x16x32_bf16 v[160:163], v[100:103], v[156:159], v[160:163]
	v_mfma_f32_16x16x32_bf16 v[156:159], v[128:131], v[156:159], v[140:143]
	v_mfma_f32_16x16x32_bf16 v[136:139], v[100:103], v[172:175], v[136:139]
	v_mfma_f32_16x16x32_bf16 v[132:135], v[128:131], v[172:175], v[132:135]
	v_mfma_f32_16x16x32_bf16 v[112:115], v[100:103], v[184:187], v[112:115]
	v_mfma_f32_16x16x32_bf16 v[108:111], v[128:131], v[184:187], v[108:111]
	v_mfma_f32_16x16x32_bf16 v[88:91], v[100:103], v[192:195], v[88:91]
	v_mfma_f32_16x16x32_bf16 v[80:83], v[128:131], v[192:195], v[80:83]
	s_setprio 0
	s_barrier
	ds_read_b128 v[140:143], v232 offset:49152
	ds_read_b128 v[152:155], v232 offset:50176
	ds_read_b128 v[164:167], v232 offset:51200
	ds_read_b128 v[172:175], v232 offset:52224
	ds_read_b128 v[180:183], v232 offset:53248
	ds_read_b128 v[184:187], v232 offset:54272
	ds_read_b128 v[188:191], v232 offset:55296
	ds_read_b128 v[192:195], v232 offset:56320
	s_add_i32 s15, s15, s54
	v_lshl_add_u64 v[196:197], v[196:197], 0, s[24:25]
	s_mov_b32 m0, s15
	global_load_lds_dwordx4 v[196:197], off
	s_add_i32 m0, s15, 0x2000
	s_add_u32 s26, s42, 0x40080
	v_lshl_add_u64 v[196:197], v[198:199], 0, s[24:25]
	s_addc_u32 s27, s43, 0
	s_add_i32 s15, s17, s54
	global_load_lds_dwordx4 v[196:197], off
	s_mov_b32 m0, s15
	v_lshl_add_u64 v[196:197], v[200:201], 0, s[24:25]
	global_load_lds_dwordx4 v216, s[26:27]
	s_add_i32 m0, s15, 0x2000
	s_nop 0
	global_load_lds_dwordx4 v220, s[26:27]
	s_mov_b32 m0, s60
	s_nop 0
	global_load_lds_dwordx4 v[196:197], off
	v_lshl_add_u64 v[196:197], v[202:203], 0, s[24:25]
	s_mov_b32 m0, s61
	s_nop 0
	global_load_lds_dwordx4 v[196:197], off
	s_waitcnt vmcnt(8)
	s_waitcnt lgkmcnt(0)
	s_barrier
	s_setprio 1
	s_waitcnt lgkmcnt(0)
	v_mfma_f32_16x16x32_bf16 v[64:67], v[68:71], v[140:143], v[64:67]
	v_mfma_f32_16x16x32_bf16 v[60:63], v[76:79], v[140:143], v[60:63]
	v_mfma_f32_16x16x32_bf16 v[48:51], v[68:71], v[164:167], v[48:51]
	v_mfma_f32_16x16x32_bf16 v[44:47], v[76:79], v[164:167], v[44:47]
	v_mfma_f32_16x16x32_bf16 v[32:35], v[68:71], v[180:183], v[32:35]
	v_mfma_f32_16x16x32_bf16 v[28:31], v[76:79], v[180:183], v[28:31]
	v_mfma_f32_16x16x32_bf16 v[16:19], v[68:71], v[188:191], v[16:19]
	v_mfma_f32_16x16x32_bf16 v[12:15], v[76:79], v[188:191], v[12:15]
	v_mfma_f32_16x16x32_bf16 v[64:67], v[72:75], v[152:155], v[64:67]
	v_mfma_f32_16x16x32_bf16 v[60:63], v[84:87], v[152:155], v[60:63]
	v_mfma_f32_16x16x32_bf16 v[48:51], v[72:75], v[172:175], v[48:51]
	v_mfma_f32_16x16x32_bf16 v[44:47], v[84:87], v[172:175], v[44:47]
	v_mfma_f32_16x16x32_bf16 v[32:35], v[72:75], v[184:187], v[32:35]
	v_mfma_f32_16x16x32_bf16 v[28:31], v[84:87], v[184:187], v[28:31]
	v_mfma_f32_16x16x32_bf16 v[16:19], v[72:75], v[192:195], v[16:19]
	v_mfma_f32_16x16x32_bf16 v[12:15], v[84:87], v[192:195], v[12:15]
	s_setprio 0
	s_setprio 1
	v_mfma_f32_16x16x32_bf16 v[56:59], v[92:95], v[140:143], v[56:59]
	v_mfma_f32_16x16x32_bf16 v[52:55], v[116:119], v[140:143], v[52:55]
	v_mfma_f32_16x16x32_bf16 v[40:43], v[92:95], v[164:167], v[40:43]
	v_mfma_f32_16x16x32_bf16 v[36:39], v[116:119], v[164:167], v[36:39]
	v_mfma_f32_16x16x32_bf16 v[24:27], v[92:95], v[180:183], v[24:27]
	v_mfma_f32_16x16x32_bf16 v[20:23], v[116:119], v[180:183], v[20:23]
	v_mfma_f32_16x16x32_bf16 v[8:11], v[92:95], v[188:191], v[8:11]
	v_mfma_f32_16x16x32_bf16 v[4:7], v[116:119], v[188:191], v[4:7]
	v_mfma_f32_16x16x32_bf16 v[56:59], v[100:103], v[152:155], v[56:59]
	v_mfma_f32_16x16x32_bf16 v[52:55], v[128:131], v[152:155], v[52:55]
	v_mfma_f32_16x16x32_bf16 v[40:43], v[100:103], v[172:175], v[40:43]
	v_mfma_f32_16x16x32_bf16 v[36:39], v[128:131], v[172:175], v[36:39]
	v_mfma_f32_16x16x32_bf16 v[24:27], v[100:103], v[184:187], v[24:27]
	v_mfma_f32_16x16x32_bf16 v[20:23], v[128:131], v[184:187], v[20:23]
	v_mfma_f32_16x16x32_bf16 v[8:11], v[100:103], v[192:195], v[8:11]
	v_mfma_f32_16x16x32_bf16 v[4:7], v[128:131], v[192:195], v[4:7]
	s_setprio 0
	s_barrier
	s_add_i32 s3, s3, 2
	s_add_u32 s38, s38, 0x100
	s_addc_u32 s39, s39, 0
	s_cmp_gt_u32 s3, 13
	s_cbranch_scc0 .LBB0_847
	s_and_b64 vcc, exec, s[10:11]
	s_cbranch_vccz .LBB0_850
	s_barrier

.LBB0_998:
	v_add_u32_e32 v144, 0x10000, v207
	v_add_u32_e32 v160, 0x14000, v207
	ds_read_b128 v[132:135], v144
	ds_read_b128 v[136:139], v144 offset:1024
	ds_read_b128 v[140:143], v144 offset:2048
	ds_read_b128 v[144:147], v144 offset:3072
	ds_read_b128 v[148:151], v160
	ds_read_b128 v[152:155], v160 offset:1024
	ds_read_b128 v[156:159], v160 offset:2048
	ds_read_b128 v[160:163], v160 offset:3072
	ds_read_b128 v[164:167], v208
	ds_read_b128 v[168:171], v208 offset:1024
	ds_read_b128 v[172:175], v208 offset:2048
	ds_read_b128 v[176:179], v208 offset:3072
	ds_read_b128 v[180:183], v208 offset:4096
	ds_read_b128 v[184:187], v208 offset:5120
	ds_read_b128 v[188:191], v208 offset:6144
	ds_read_b128 v[192:195], v208 offset:7168
	s_add_i32 s15, s13, 0x100
	s_and_b64 s[26:27], s[38:39], s[36:37]
	s_and_b64 s[34:35], s[26:27], exec
	s_cselect_b32 s21, s19, s23
	s_cselect_b32 s28, s18, s22
	s_and_b64 s[34:35], s[38:39], exec
	s_cselect_b32 s15, 0, s15
	s_cselect_b32 s35, 0, 0
	s_add_u32 s42, s28, s15
	s_addc_u32 s43, s21, s35
	s_add_i32 s39, 0, 0x10000
	s_and_b64 s[26:27], s[26:27], exec
	s_cselect_b32 s21, s17, s1
	s_cselect_b32 s26, s16, s0
	s_add_i32 s46, 0, 0x14000
	s_add_u32 s13, s0, s13
	s_addc_u32 s27, s1, 0
	s_add_u32 s50, s13, 0x80080
	s_addc_u32 s51, s27, 0
	s_add_i32 s34, s39, s8
	s_add_i32 m0, s57, 0xc000
	s_add_i32 s47, s57, 0xe000
	s_add_i32 s27, s34, 0x2000
	s_add_u32 s48, s42, 0x10000
	s_addc_u32 s49, s43, 0
	s_add_i32 s33, s46, s8
	s_add_i32 s28, s33, 0x2000
	s_add_u32 s44, s26, s15
	s_addc_u32 s45, s21, s35
	s_add_i32 s26, 0, 0x18000
	s_add_i32 s21, 0, 0x1c000
	s_add_u32 s40, s44, 0x80000
	s_addc_u32 s41, s45, 0
	s_add_i32 s15, s26, s8
	s_add_i32 s13, s15, 0x2000
	s_add_u32 s38, s42, 0x10080
	s_addc_u32 s39, s43, 0
	s_add_i32 s46, s21, s8
	s_add_i32 s35, s46, 0x2000
	global_load_lds_dwordx4 v2, s[50:51]
	s_mov_b32 m0, s47
	v_mov_b32_e32 v199, v3
	global_load_lds_dwordx4 v198, s[50:51]
	s_waitcnt vmcnt(8)
	s_waitcnt lgkmcnt(0)
	s_barrier
	s_setprio 1
	s_waitcnt lgkmcnt(0)
	v_mfma_f32_16x16x32_bf16 v[128:131], v[132:135], v[164:167], v[128:131]
	v_mfma_f32_16x16x32_bf16 v[124:127], v[140:143], v[164:167], v[124:127]
	v_mfma_f32_16x16x32_bf16 v[112:115], v[132:135], v[172:175], v[112:115]
	v_mfma_f32_16x16x32_bf16 v[108:111], v[140:143], v[172:175], v[108:111]
	v_mfma_f32_16x16x32_bf16 v[96:99], v[132:135], v[180:183], v[96:99]
	v_mfma_f32_16x16x32_bf16 v[92:95], v[140:143], v[180:183], v[92:95]
	v_mfma_f32_16x16x32_bf16 v[80:83], v[132:135], v[188:191], v[80:83]
	v_mfma_f32_16x16x32_bf16 v[76:79], v[140:143], v[188:191], v[76:79]
	v_mfma_f32_16x16x32_bf16 v[128:131], v[136:139], v[168:171], v[128:131]
	v_mfma_f32_16x16x32_bf16 v[124:127], v[144:147], v[168:171], v[124:127]
	v_mfma_f32_16x16x32_bf16 v[112:115], v[136:139], v[176:179], v[112:115]
	v_mfma_f32_16x16x32_bf16 v[108:111], v[144:147], v[176:179], v[108:111]
	v_mfma_f32_16x16x32_bf16 v[96:99], v[136:139], v[184:187], v[96:99]
	v_mfma_f32_16x16x32_bf16 v[92:95], v[144:147], v[184:187], v[92:95]
	v_mfma_f32_16x16x32_bf16 v[80:83], v[136:139], v[192:195], v[80:83]
	v_mfma_f32_16x16x32_bf16 v[76:79], v[144:147], v[192:195], v[76:79]
	s_setprio 0
	s_setprio 1
	v_mfma_f32_16x16x32_bf16 v[120:123], v[148:151], v[164:167], v[120:123]
	v_mfma_f32_16x16x32_bf16 v[116:119], v[156:159], v[164:167], v[116:119]
	v_mfma_f32_16x16x32_bf16 v[104:107], v[148:151], v[172:175], v[104:107]
	v_mfma_f32_16x16x32_bf16 v[100:103], v[156:159], v[172:175], v[100:103]
	v_mfma_f32_16x16x32_bf16 v[88:91], v[148:151], v[180:183], v[88:91]
	v_mfma_f32_16x16x32_bf16 v[84:87], v[156:159], v[180:183], v[84:87]
	v_mfma_f32_16x16x32_bf16 v[72:75], v[148:151], v[188:191], v[72:75]
	v_mfma_f32_16x16x32_bf16 v[68:71], v[156:159], v[188:191], v[68:71]
	v_mfma_f32_16x16x32_bf16 v[120:123], v[152:155], v[168:171], v[120:123]
	v_mfma_f32_16x16x32_bf16 v[116:119], v[160:163], v[168:171], v[116:119]
	v_mfma_f32_16x16x32_bf16 v[104:107], v[152:155], v[176:179], v[104:107]
	v_mfma_f32_16x16x32_bf16 v[100:103], v[160:163], v[176:179], v[100:103]
	v_mfma_f32_16x16x32_bf16 v[88:91], v[152:155], v[184:187], v[88:91]
	v_mfma_f32_16x16x32_bf16 v[84:87], v[160:163], v[184:187], v[84:87]
	v_mfma_f32_16x16x32_bf16 v[72:75], v[152:155], v[192:195], v[72:75]
	v_mfma_f32_16x16x32_bf16 v[68:71], v[160:163], v[192:195], v[68:71]
	s_setprio 0
	s_barrier
	ds_read_b128 v[164:167], v208 offset:16384
	ds_read_b128 v[168:171], v208 offset:17408
	ds_read_b128 v[172:175], v208 offset:18432
	ds_read_b128 v[176:179], v208 offset:19456
	ds_read_b128 v[180:183], v208 offset:20480
	ds_read_b128 v[184:187], v208 offset:21504
	ds_read_b128 v[188:191], v208 offset:22528
	ds_read_b128 v[192:195], v208 offset:23552
	s_mov_b32 m0, s34
	global_load_lds_dwordx4 v196, s[42:43]
	s_mov_b32 m0, s27
	v_mov_b32_e32 v197, v3
	global_load_lds_dwordx4 v200, s[42:43]
	s_mov_b32 m0, s33
	v_mov_b32_e32 v201, v3
	global_load_lds_dwordx4 v196, s[48:49]
	s_mov_b32 m0, s28
	v_lshl_add_u64 v[202:203], s[42:43], 0, v[196:197]
	global_load_lds_dwordx4 v200, s[48:49]
	s_mov_b32 m0, s57
	v_lshl_add_u64 v[204:205], s[42:43], 0, v[200:201]
	global_load_lds_dwordx4 v2, s[44:45]
	s_mov_b32 m0, s58
	v_lshl_add_u64 v[210:211], s[44:45], 0, v[2:3]
	global_load_lds_dwordx4 v198, s[44:45]
	s_waitcnt vmcnt(8)
	s_waitcnt lgkmcnt(0)
	v_lshl_add_u64 v[212:213], s[44:45], 0, v[198:199]
	s_barrier
	s_setprio 1
	s_waitcnt lgkmcnt(0)
	v_mfma_f32_16x16x32_bf16 v[64:67], v[132:135], v[164:167], v[64:67]
	v_mfma_f32_16x16x32_bf16 v[60:63], v[140:143], v[164:167], v[60:63]
	v_mfma_f32_16x16x32_bf16 v[48:51], v[132:135], v[172:175], v[48:51]
	v_mfma_f32_16x16x32_bf16 v[44:47], v[140:143], v[172:175], v[44:47]
	v_mfma_f32_16x16x32_bf16 v[32:35], v[132:135], v[180:183], v[32:35]
	v_mfma_f32_16x16x32_bf16 v[28:31], v[140:143], v[180:183], v[28:31]
	v_mfma_f32_16x16x32_bf16 v[16:19], v[132:135], v[188:191], v[16:19]
	v_mfma_f32_16x16x32_bf16 v[12:15], v[140:143], v[188:191], v[12:15]
	v_mfma_f32_16x16x32_bf16 v[64:67], v[136:139], v[168:171], v[64:67]
	v_mfma_f32_16x16x32_bf16 v[60:63], v[144:147], v[168:171], v[60:63]
	v_mfma_f32_16x16x32_bf16 v[48:51], v[136:139], v[176:179], v[48:51]
	v_mfma_f32_16x16x32_bf16 v[44:47], v[144:147], v[176:179], v[44:47]
	v_mfma_f32_16x16x32_bf16 v[32:35], v[136:139], v[184:187], v[32:35]
	v_mfma_f32_16x16x32_bf16 v[28:31], v[144:147], v[184:187], v[28:31]
	v_mfma_f32_16x16x32_bf16 v[16:19], v[136:139], v[192:195], v[16:19]
	v_mfma_f32_16x16x32_bf16 v[12:15], v[144:147], v[192:195], v[12:15]
	s_setprio 0
	s_setprio 1
	v_mfma_f32_16x16x32_bf16 v[56:59], v[148:151], v[164:167], v[56:59]
	v_mfma_f32_16x16x32_bf16 v[52:55], v[156:159], v[164:167], v[52:55]
	v_mfma_f32_16x16x32_bf16 v[40:43], v[148:151], v[172:175], v[40:43]
	v_mfma_f32_16x16x32_bf16 v[36:39], v[156:159], v[172:175], v[36:39]
	v_mfma_f32_16x16x32_bf16 v[24:27], v[148:151], v[180:183], v[24:27]
	v_mfma_f32_16x16x32_bf16 v[20:23], v[156:159], v[180:183], v[20:23]
	v_mfma_f32_16x16x32_bf16 v[8:11], v[148:151], v[188:191], v[8:11]
	v_mfma_f32_16x16x32_bf16 v[4:7], v[156:159], v[188:191], v[4:7]
	v_mfma_f32_16x16x32_bf16 v[56:59], v[152:155], v[168:171], v[56:59]
	v_mfma_f32_16x16x32_bf16 v[52:55], v[160:163], v[168:171], v[52:55]
	v_mfma_f32_16x16x32_bf16 v[40:43], v[152:155], v[176:179], v[40:43]
	v_mfma_f32_16x16x32_bf16 v[36:39], v[160:163], v[176:179], v[36:39]
	v_mfma_f32_16x16x32_bf16 v[24:27], v[152:155], v[184:187], v[24:27]
	v_mfma_f32_16x16x32_bf16 v[20:23], v[160:163], v[184:187], v[20:23]
	v_mfma_f32_16x16x32_bf16 v[8:11], v[152:155], v[192:195], v[8:11]
	v_mfma_f32_16x16x32_bf16 v[4:7], v[160:163], v[192:195], v[4:7]
	s_setprio 0
	s_barrier
	v_add_u32_e32 v144, s26, v207
	v_add_u32_e32 v160, s21, v207
	ds_read_b128 v[132:135], v144
	ds_read_b128 v[136:139], v144 offset:1024
	ds_read_b128 v[140:143], v144 offset:2048
	ds_read_b128 v[144:147], v144 offset:3072
	ds_read_b128 v[148:151], v160
	ds_read_b128 v[152:155], v160 offset:1024
	ds_read_b128 v[156:159], v160 offset:2048
	ds_read_b128 v[160:163], v160 offset:3072
	ds_read_b128 v[164:167], v208 offset:32768
	ds_read_b128 v[168:171], v208 offset:33792
	ds_read_b128 v[172:175], v208 offset:34816
	ds_read_b128 v[176:179], v208 offset:35840
	ds_read_b128 v[180:183], v208 offset:36864
	ds_read_b128 v[184:187], v208 offset:37888
	ds_read_b128 v[188:191], v208 offset:38912
	ds_read_b128 v[192:195], v208 offset:39936
	s_mov_b32 m0, s59
	global_load_lds_dwordx4 v2, s[40:41]
	s_mov_b32 m0, s60
	s_nop 0
	global_load_lds_dwordx4 v198, s[40:41]
	s_waitcnt vmcnt(8)
	s_waitcnt lgkmcnt(0)
	s_barrier
	s_setprio 1
	s_waitcnt lgkmcnt(0)
	v_mfma_f32_16x16x32_bf16 v[128:131], v[132:135], v[164:167], v[128:131]
	v_mfma_f32_16x16x32_bf16 v[124:127], v[140:143], v[164:167], v[124:127]
	v_mfma_f32_16x16x32_bf16 v[112:115], v[132:135], v[172:175], v[112:115]
	v_mfma_f32_16x16x32_bf16 v[108:111], v[140:143], v[172:175], v[108:111]
	v_mfma_f32_16x16x32_bf16 v[96:99], v[132:135], v[180:183], v[96:99]
	v_mfma_f32_16x16x32_bf16 v[92:95], v[140:143], v[180:183], v[92:95]
	v_mfma_f32_16x16x32_bf16 v[80:83], v[132:135], v[188:191], v[80:83]
	v_mfma_f32_16x16x32_bf16 v[76:79], v[140:143], v[188:191], v[76:79]
	v_mfma_f32_16x16x32_bf16 v[128:131], v[136:139], v[168:171], v[128:131]
	v_mfma_f32_16x16x32_bf16 v[124:127], v[144:147], v[168:171], v[124:127]
	v_mfma_f32_16x16x32_bf16 v[112:115], v[136:139], v[176:179], v[112:115]
	v_mfma_f32_16x16x32_bf16 v[108:111], v[144:147], v[176:179], v[108:111]
	v_mfma_f32_16x16x32_bf16 v[96:99], v[136:139], v[184:187], v[96:99]
	v_mfma_f32_16x16x32_bf16 v[92:95], v[144:147], v[184:187], v[92:95]
	v_mfma_f32_16x16x32_bf16 v[80:83], v[136:139], v[192:195], v[80:83]
	v_mfma_f32_16x16x32_bf16 v[76:79], v[144:147], v[192:195], v[76:79]
	s_setprio 0
	s_setprio 1
	v_mfma_f32_16x16x32_bf16 v[120:123], v[148:151], v[164:167], v[120:123]
	v_mfma_f32_16x16x32_bf16 v[116:119], v[156:159], v[164:167], v[116:119]
	v_mfma_f32_16x16x32_bf16 v[104:107], v[148:151], v[172:175], v[104:107]
	v_mfma_f32_16x16x32_bf16 v[100:103], v[156:159], v[172:175], v[100:103]
	v_mfma_f32_16x16x32_bf16 v[88:91], v[148:151], v[180:183], v[88:91]
	v_mfma_f32_16x16x32_bf16 v[84:87], v[156:159], v[180:183], v[84:87]
	v_mfma_f32_16x16x32_bf16 v[72:75], v[148:151], v[188:191], v[72:75]
	v_mfma_f32_16x16x32_bf16 v[68:71], v[156:159], v[188:191], v[68:71]
	v_mfma_f32_16x16x32_bf16 v[120:123], v[152:155], v[168:171], v[120:123]
	v_mfma_f32_16x16x32_bf16 v[116:119], v[160:163], v[168:171], v[116:119]
	v_mfma_f32_16x16x32_bf16 v[104:107], v[152:155], v[176:179], v[104:107]
	v_mfma_f32_16x16x32_bf16 v[100:103], v[160:163], v[176:179], v[100:103]
	v_mfma_f32_16x16x32_bf16 v[88:91], v[152:155], v[184:187], v[88:91]
	v_mfma_f32_16x16x32_bf16 v[84:87], v[160:163], v[184:187], v[84:87]
	v_mfma_f32_16x16x32_bf16 v[72:75], v[152:155], v[192:195], v[72:75]
	v_mfma_f32_16x16x32_bf16 v[68:71], v[160:163], v[192:195], v[68:71]
	s_setprio 0
	s_barrier
	ds_read_b128 v[164:167], v208 offset:49152
	ds_read_b128 v[168:171], v208 offset:50176
	ds_read_b128 v[172:175], v208 offset:51200
	ds_read_b128 v[176:179], v208 offset:52224
	ds_read_b128 v[180:183], v208 offset:53248
	ds_read_b128 v[184:187], v208 offset:54272
	ds_read_b128 v[188:191], v208 offset:55296
	ds_read_b128 v[192:195], v208 offset:56320
	s_mov_b32 m0, s15
	v_lshl_add_u64 v[202:203], v[202:203], 0, s[24:25]
	global_load_lds_dwordx4 v[202:203], off
	v_lshl_add_u64 v[202:203], v[204:205], 0, s[24:25]
	s_mov_b32 m0, s13
	s_nop 0
	global_load_lds_dwordx4 v[202:203], off
	s_mov_b32 m0, s46
	v_lshl_add_u64 v[202:203], v[210:211], 0, s[24:25]
	global_load_lds_dwordx4 v196, s[38:39]
	s_mov_b32 m0, s35
	s_nop 0
	global_load_lds_dwordx4 v200, s[38:39]
	s_mov_b32 m0, s63
	s_nop 0
	global_load_lds_dwordx4 v[202:203], off
	v_lshl_add_u64 v[202:203], v[212:213], 0, s[24:25]
	s_mov_b32 m0, s64
	s_nop 0
	global_load_lds_dwordx4 v[202:203], off
	s_waitcnt vmcnt(8)
	s_waitcnt lgkmcnt(0)
	s_barrier
	s_setprio 1
	s_waitcnt lgkmcnt(0)
	v_mfma_f32_16x16x32_bf16 v[64:67], v[132:135], v[164:167], v[64:67]
	v_mfma_f32_16x16x32_bf16 v[60:63], v[140:143], v[164:167], v[60:63]
	v_mfma_f32_16x16x32_bf16 v[48:51], v[132:135], v[172:175], v[48:51]
	v_mfma_f32_16x16x32_bf16 v[44:47], v[140:143], v[172:175], v[44:47]
	v_mfma_f32_16x16x32_bf16 v[32:35], v[132:135], v[180:183], v[32:35]
	v_mfma_f32_16x16x32_bf16 v[28:31], v[140:143], v[180:183], v[28:31]
	v_mfma_f32_16x16x32_bf16 v[16:19], v[132:135], v[188:191], v[16:19]
	v_mfma_f32_16x16x32_bf16 v[12:15], v[140:143], v[188:191], v[12:15]
	v_mfma_f32_16x16x32_bf16 v[64:67], v[136:139], v[168:171], v[64:67]
	v_mfma_f32_16x16x32_bf16 v[60:63], v[144:147], v[168:171], v[60:63]
	v_mfma_f32_16x16x32_bf16 v[48:51], v[136:139], v[176:179], v[48:51]
	v_mfma_f32_16x16x32_bf16 v[44:47], v[144:147], v[176:179], v[44:47]
	v_mfma_f32_16x16x32_bf16 v[32:35], v[136:139], v[184:187], v[32:35]
	v_mfma_f32_16x16x32_bf16 v[28:31], v[144:147], v[184:187], v[28:31]
	v_mfma_f32_16x16x32_bf16 v[16:19], v[136:139], v[192:195], v[16:19]
	v_mfma_f32_16x16x32_bf16 v[12:15], v[144:147], v[192:195], v[12:15]
	s_setprio 0
	s_setprio 1
	v_mfma_f32_16x16x32_bf16 v[56:59], v[148:151], v[164:167], v[56:59]
	v_mfma_f32_16x16x32_bf16 v[52:55], v[156:159], v[164:167], v[52:55]
	v_mfma_f32_16x16x32_bf16 v[40:43], v[148:151], v[172:175], v[40:43]
	v_mfma_f32_16x16x32_bf16 v[36:39], v[156:159], v[172:175], v[36:39]
	v_mfma_f32_16x16x32_bf16 v[24:27], v[148:151], v[180:183], v[24:27]
	v_mfma_f32_16x16x32_bf16 v[20:23], v[156:159], v[180:183], v[20:23]
	v_mfma_f32_16x16x32_bf16 v[8:11], v[148:151], v[188:191], v[8:11]
	v_mfma_f32_16x16x32_bf16 v[4:7], v[156:159], v[188:191], v[4:7]
	v_mfma_f32_16x16x32_bf16 v[56:59], v[152:155], v[168:171], v[56:59]
	v_mfma_f32_16x16x32_bf16 v[52:55], v[160:163], v[168:171], v[52:55]
	v_mfma_f32_16x16x32_bf16 v[40:43], v[152:155], v[176:179], v[40:43]
	v_mfma_f32_16x16x32_bf16 v[36:39], v[160:163], v[176:179], v[36:39]
	v_mfma_f32_16x16x32_bf16 v[24:27], v[152:155], v[184:187], v[24:27]
	v_mfma_f32_16x16x32_bf16 v[20:23], v[160:163], v[184:187], v[20:23]
	v_mfma_f32_16x16x32_bf16 v[8:11], v[152:155], v[192:195], v[8:11]
	v_mfma_f32_16x16x32_bf16 v[4:7], v[160:163], v[192:195], v[4:7]
	s_setprio 0
	s_barrier
	s_andn2_b64 vcc, exec, s[30:31]
	s_mov_b64 s[38:39], -1
	s_mov_b64 s[30:31], 0
	s_movk_i32 s13, 0x100
	s_cbranch_vccz .LBB0_998
	s_and_b64 vcc, exec, s[10:11]
	s_cbranch_vccz .LBB0_1001
	s_barrier

.LBB0_1033:
	v_add_u32_e32 v133, 0x10000, v143
	ds_read_b128 v[138:141], v133
	ds_read_b128 v[146:149], v133 offset:1024
	ds_read_b128 v[150:153], v133 offset:2048
	ds_read_b128 v[154:157], v133 offset:3072
	v_add_u32_e32 v133, 0x14000, v143
	ds_read_b128 v[158:161], v133
	ds_read_b128 v[162:165], v133 offset:1024
	ds_read_b128 v[166:169], v133 offset:2048
	ds_read_b128 v[170:173], v133 offset:3072
	ds_read_b128 v[174:177], v144
	ds_read_b128 v[178:181], v144 offset:1024
	ds_read_b128 v[182:185], v144 offset:2048
	ds_read_b128 v[186:189], v144 offset:3072
	ds_read_b128 v[190:193], v144 offset:4096
	ds_read_b128 v[194:197], v144 offset:5120
	ds_read_b128 v[198:201], v144 offset:6144
	ds_read_b128 v[202:205], v144 offset:7168
	s_cmp_eq_u32 s61, s19
	s_cselect_b64 s[26:27], -1, 0
	s_add_i32 s19, s19, 2
	s_add_u32 s28, s42, 0xfff80080
	s_addc_u32 s31, s43, -1
	s_and_b64 s[34:35], s[26:27], exec
	s_cselect_b32 s34, s20, s40
	s_cselect_b32 s28, 0, s28
	s_cselect_b32 s33, s21, s41
	s_cselect_b32 s31, 0, s31
	s_add_u32 s44, s34, s28
	s_addc_u32 s45, s33, s31
	s_add_i32 s33, 0, 0x10000
	s_and_b64 s[26:27], s[26:27], s[0:1]
	s_and_b64 s[26:27], s[26:27], exec
	s_cselect_b32 s34, s23, s39
	s_cselect_b32 s35, s22, s38
	s_add_i32 s46, 0, 0x14000
	s_add_i32 m0, s53, 0xc000
	s_add_u32 s26, s38, s42
	s_addc_u32 s27, s39, s43
	global_load_lds_dwordx4 v2, s[26:27]
	s_add_i32 m0, s53, 0xe000
	v_mov_b32_e32 v135, v3
	global_load_lds_dwordx4 v134, s[26:27]
	s_waitcnt vmcnt(8)
	s_waitcnt lgkmcnt(0)
	s_barrier
	s_setprio 1
	s_waitcnt lgkmcnt(0)
	v_mfma_f32_16x16x32_bf16 v[124:127], v[138:141], v[174:177], v[124:127]
	v_mfma_f32_16x16x32_bf16 v[128:131], v[150:153], v[174:177], v[128:131]
	v_mfma_f32_16x16x32_bf16 v[112:115], v[138:141], v[182:185], v[112:115]
	v_mfma_f32_16x16x32_bf16 v[108:111], v[150:153], v[182:185], v[108:111]
	v_mfma_f32_16x16x32_bf16 v[96:99], v[138:141], v[190:193], v[96:99]
	v_mfma_f32_16x16x32_bf16 v[92:95], v[150:153], v[190:193], v[92:95]
	v_mfma_f32_16x16x32_bf16 v[80:83], v[138:141], v[198:201], v[80:83]
	v_mfma_f32_16x16x32_bf16 v[76:79], v[150:153], v[198:201], v[76:79]
	v_mfma_f32_16x16x32_bf16 v[124:127], v[146:149], v[178:181], v[124:127]
	v_mfma_f32_16x16x32_bf16 v[128:131], v[154:157], v[178:181], v[128:131]
	v_mfma_f32_16x16x32_bf16 v[112:115], v[146:149], v[186:189], v[112:115]
	v_mfma_f32_16x16x32_bf16 v[108:111], v[154:157], v[186:189], v[108:111]
	v_mfma_f32_16x16x32_bf16 v[96:99], v[146:149], v[194:197], v[96:99]
	v_mfma_f32_16x16x32_bf16 v[92:95], v[154:157], v[194:197], v[92:95]
	v_mfma_f32_16x16x32_bf16 v[80:83], v[146:149], v[202:205], v[80:83]
	v_mfma_f32_16x16x32_bf16 v[76:79], v[154:157], v[202:205], v[76:79]
	s_setprio 0
	s_setprio 1
	v_mfma_f32_16x16x32_bf16 v[120:123], v[158:161], v[174:177], v[120:123]
	v_mfma_f32_16x16x32_bf16 v[116:119], v[166:169], v[174:177], v[116:119]
	v_mfma_f32_16x16x32_bf16 v[104:107], v[158:161], v[182:185], v[104:107]
	v_mfma_f32_16x16x32_bf16 v[100:103], v[166:169], v[182:185], v[100:103]
	v_mfma_f32_16x16x32_bf16 v[88:91], v[158:161], v[190:193], v[88:91]
	v_mfma_f32_16x16x32_bf16 v[84:87], v[166:169], v[190:193], v[84:87]
	v_mfma_f32_16x16x32_bf16 v[72:75], v[158:161], v[198:201], v[72:75]
	v_mfma_f32_16x16x32_bf16 v[68:71], v[166:169], v[198:201], v[68:71]
	v_mfma_f32_16x16x32_bf16 v[120:123], v[162:165], v[178:181], v[120:123]
	v_mfma_f32_16x16x32_bf16 v[116:119], v[170:173], v[178:181], v[116:119]
	v_mfma_f32_16x16x32_bf16 v[104:107], v[162:165], v[186:189], v[104:107]
	v_mfma_f32_16x16x32_bf16 v[100:103], v[170:173], v[186:189], v[100:103]
	v_mfma_f32_16x16x32_bf16 v[88:91], v[162:165], v[194:197], v[88:91]
	v_mfma_f32_16x16x32_bf16 v[84:87], v[170:173], v[194:197], v[84:87]
	v_mfma_f32_16x16x32_bf16 v[72:75], v[162:165], v[202:205], v[72:75]
	v_mfma_f32_16x16x32_bf16 v[68:71], v[170:173], v[202:205], v[68:71]
	s_setprio 0
	s_barrier
	ds_read_b128 v[174:177], v144 offset:16384
	ds_read_b128 v[178:181], v144 offset:17408
	ds_read_b128 v[182:185], v144 offset:18432
	ds_read_b128 v[186:189], v144 offset:19456
	ds_read_b128 v[190:193], v144 offset:20480
	ds_read_b128 v[194:197], v144 offset:21504
	ds_read_b128 v[198:201], v144 offset:22528
	ds_read_b128 v[202:205], v144 offset:23552
	s_add_i32 s26, s33, s8
	s_mov_b32 m0, s26
	global_load_lds_dwordx4 v132, s[44:45]
	s_add_i32 m0, s26, 0x2000
	s_add_u32 s26, s44, s10
	s_addc_u32 s27, s45, s11
	s_add_i32 s33, s46, s8
	global_load_lds_dwordx4 v136, s[44:45]
	s_mov_b32 m0, s33
	v_mov_b32_e32 v133, v3
	v_mov_b32_e32 v137, v3
	global_load_lds_dwordx4 v132, s[26:27]
	s_add_i32 m0, s33, 0x2000
	v_lshl_add_u64 v[206:207], s[44:45], 0, v[132:133]
	v_lshl_add_u64 v[208:209], s[44:45], 0, v[136:137]
	s_add_u32 s44, s35, s28
	global_load_lds_dwordx4 v136, s[26:27]
	s_addc_u32 s45, s34, s31
	s_mov_b32 m0, s53
	v_lshl_add_u64 v[210:211], s[26:27], 0, v[132:133]
	global_load_lds_dwordx4 v2, s[44:45]
	s_mov_b32 m0, s54
	v_lshl_add_u64 v[212:213], s[26:27], 0, v[136:137]
	global_load_lds_dwordx4 v134, s[44:45]
	s_waitcnt vmcnt(8)
	s_waitcnt lgkmcnt(0)
	v_lshl_add_u64 v[214:215], s[44:45], 0, v[2:3]
	v_lshl_add_u64 v[216:217], s[44:45], 0, v[134:135]
	s_barrier
	s_setprio 1
	s_waitcnt lgkmcnt(0)
	v_mfma_f32_16x16x32_bf16 v[64:67], v[138:141], v[174:177], v[64:67]
	v_mfma_f32_16x16x32_bf16 v[60:63], v[150:153], v[174:177], v[60:63]
	v_mfma_f32_16x16x32_bf16 v[48:51], v[138:141], v[182:185], v[48:51]
	v_mfma_f32_16x16x32_bf16 v[44:47], v[150:153], v[182:185], v[44:47]
	v_mfma_f32_16x16x32_bf16 v[32:35], v[138:141], v[190:193], v[32:35]
	v_mfma_f32_16x16x32_bf16 v[28:31], v[150:153], v[190:193], v[28:31]
	v_mfma_f32_16x16x32_bf16 v[16:19], v[138:141], v[198:201], v[16:19]
	v_mfma_f32_16x16x32_bf16 v[12:15], v[150:153], v[198:201], v[12:15]
	v_mfma_f32_16x16x32_bf16 v[64:67], v[146:149], v[178:181], v[64:67]
	v_mfma_f32_16x16x32_bf16 v[60:63], v[154:157], v[178:181], v[60:63]
	v_mfma_f32_16x16x32_bf16 v[48:51], v[146:149], v[186:189], v[48:51]
	v_mfma_f32_16x16x32_bf16 v[44:47], v[154:157], v[186:189], v[44:47]
	v_mfma_f32_16x16x32_bf16 v[32:35], v[146:149], v[194:197], v[32:35]
	v_mfma_f32_16x16x32_bf16 v[28:31], v[154:157], v[194:197], v[28:31]
	v_mfma_f32_16x16x32_bf16 v[16:19], v[146:149], v[202:205], v[16:19]
	v_mfma_f32_16x16x32_bf16 v[12:15], v[154:157], v[202:205], v[12:15]
	s_setprio 0
	s_setprio 1
	v_mfma_f32_16x16x32_bf16 v[56:59], v[158:161], v[174:177], v[56:59]
	v_mfma_f32_16x16x32_bf16 v[52:55], v[166:169], v[174:177], v[52:55]
	v_mfma_f32_16x16x32_bf16 v[40:43], v[158:161], v[182:185], v[40:43]
	v_mfma_f32_16x16x32_bf16 v[36:39], v[166:169], v[182:185], v[36:39]
	v_mfma_f32_16x16x32_bf16 v[24:27], v[158:161], v[190:193], v[24:27]
	v_mfma_f32_16x16x32_bf16 v[20:23], v[166:169], v[190:193], v[20:23]
	v_mfma_f32_16x16x32_bf16 v[8:11], v[158:161], v[198:201], v[8:11]
	v_mfma_f32_16x16x32_bf16 v[4:7], v[166:169], v[198:201], v[4:7]
	v_mfma_f32_16x16x32_bf16 v[56:59], v[162:165], v[178:181], v[56:59]
	v_mfma_f32_16x16x32_bf16 v[52:55], v[170:173], v[178:181], v[52:55]
	v_mfma_f32_16x16x32_bf16 v[40:43], v[162:165], v[186:189], v[40:43]
	v_mfma_f32_16x16x32_bf16 v[36:39], v[170:173], v[186:189], v[36:39]
	v_mfma_f32_16x16x32_bf16 v[24:27], v[162:165], v[194:197], v[24:27]
	v_mfma_f32_16x16x32_bf16 v[20:23], v[170:173], v[194:197], v[20:23]
	v_mfma_f32_16x16x32_bf16 v[8:11], v[162:165], v[202:205], v[8:11]
	v_mfma_f32_16x16x32_bf16 v[4:7], v[170:173], v[202:205], v[4:7]
	s_setprio 0
	s_barrier
	v_add_u32_e32 v133, 0x18000, v143
	ds_read_b128 v[138:141], v133
	ds_read_b128 v[146:149], v133 offset:1024
	ds_read_b128 v[150:153], v133 offset:2048
	ds_read_b128 v[154:157], v133 offset:3072
	v_add_u32_e32 v133, 0x1c000, v143
	ds_read_b128 v[158:161], v133
	ds_read_b128 v[162:165], v133 offset:1024
	ds_read_b128 v[166:169], v133 offset:2048
	ds_read_b128 v[170:173], v133 offset:3072
	ds_read_b128 v[174:177], v144 offset:32768
	ds_read_b128 v[178:181], v144 offset:33792
	ds_read_b128 v[182:185], v144 offset:34816
	ds_read_b128 v[186:189], v144 offset:35840
	ds_read_b128 v[190:193], v144 offset:36864
	ds_read_b128 v[194:197], v144 offset:37888
	ds_read_b128 v[198:201], v144 offset:38912
	ds_read_b128 v[202:205], v144 offset:39936
	s_add_i32 s28, 0, 0x18000
	s_add_i32 s31, 0, 0x1c000
	s_add_u32 s26, s44, 0x80000
	s_addc_u32 s27, s45, 0
	s_mov_b32 m0, s55
	global_load_lds_dwordx4 v2, s[26:27]
	s_mov_b32 m0, s56
	s_nop 0
	global_load_lds_dwordx4 v134, s[26:27]
	s_waitcnt vmcnt(8)
	s_waitcnt lgkmcnt(0)
	s_barrier
	s_setprio 1
	s_waitcnt lgkmcnt(0)
	v_mfma_f32_16x16x32_bf16 v[124:127], v[138:141], v[174:177], v[124:127]
	v_mfma_f32_16x16x32_bf16 v[128:131], v[150:153], v[174:177], v[128:131]
	v_mfma_f32_16x16x32_bf16 v[112:115], v[138:141], v[182:185], v[112:115]
	v_mfma_f32_16x16x32_bf16 v[108:111], v[150:153], v[182:185], v[108:111]
	v_mfma_f32_16x16x32_bf16 v[96:99], v[138:141], v[190:193], v[96:99]
	v_mfma_f32_16x16x32_bf16 v[92:95], v[150:153], v[190:193], v[92:95]
	v_mfma_f32_16x16x32_bf16 v[80:83], v[138:141], v[198:201], v[80:83]
	v_mfma_f32_16x16x32_bf16 v[76:79], v[150:153], v[198:201], v[76:79]
	v_mfma_f32_16x16x32_bf16 v[124:127], v[146:149], v[178:181], v[124:127]
	v_mfma_f32_16x16x32_bf16 v[128:131], v[154:157], v[178:181], v[128:131]
	v_mfma_f32_16x16x32_bf16 v[112:115], v[146:149], v[186:189], v[112:115]
	v_mfma_f32_16x16x32_bf16 v[108:111], v[154:157], v[186:189], v[108:111]
	v_mfma_f32_16x16x32_bf16 v[96:99], v[146:149], v[194:197], v[96:99]
	v_mfma_f32_16x16x32_bf16 v[92:95], v[154:157], v[194:197], v[92:95]
	v_mfma_f32_16x16x32_bf16 v[80:83], v[146:149], v[202:205], v[80:83]
	v_mfma_f32_16x16x32_bf16 v[76:79], v[154:157], v[202:205], v[76:79]
	s_setprio 0
	s_setprio 1
	v_mfma_f32_16x16x32_bf16 v[120:123], v[158:161], v[174:177], v[120:123]
	v_mfma_f32_16x16x32_bf16 v[116:119], v[166:169], v[174:177], v[116:119]
	v_mfma_f32_16x16x32_bf16 v[104:107], v[158:161], v[182:185], v[104:107]
	v_mfma_f32_16x16x32_bf16 v[100:103], v[166:169], v[182:185], v[100:103]
	v_mfma_f32_16x16x32_bf16 v[88:91], v[158:161], v[190:193], v[88:91]
	v_mfma_f32_16x16x32_bf16 v[84:87], v[166:169], v[190:193], v[84:87]
	v_mfma_f32_16x16x32_bf16 v[72:75], v[158:161], v[198:201], v[72:75]
	v_mfma_f32_16x16x32_bf16 v[68:71], v[166:169], v[198:201], v[68:71]
	v_mfma_f32_16x16x32_bf16 v[120:123], v[162:165], v[178:181], v[120:123]
	v_mfma_f32_16x16x32_bf16 v[116:119], v[170:173], v[178:181], v[116:119]
	v_mfma_f32_16x16x32_bf16 v[104:107], v[162:165], v[186:189], v[104:107]
	v_mfma_f32_16x16x32_bf16 v[100:103], v[170:173], v[186:189], v[100:103]
	v_mfma_f32_16x16x32_bf16 v[88:91], v[162:165], v[194:197], v[88:91]
	v_mfma_f32_16x16x32_bf16 v[84:87], v[170:173], v[194:197], v[84:87]
	v_mfma_f32_16x16x32_bf16 v[72:75], v[162:165], v[202:205], v[72:75]
	v_mfma_f32_16x16x32_bf16 v[68:71], v[170:173], v[202:205], v[68:71]
	s_setprio 0
	s_barrier
	ds_read_b128 v[174:177], v144 offset:49152
	ds_read_b128 v[178:181], v144 offset:50176
	ds_read_b128 v[182:185], v144 offset:51200
	ds_read_b128 v[186:189], v144 offset:52224
	ds_read_b128 v[190:193], v144 offset:53248
	ds_read_b128 v[194:197], v144 offset:54272
	ds_read_b128 v[198:201], v144 offset:55296
	ds_read_b128 v[202:205], v144 offset:56320
	s_add_i32 s26, s28, s8
	v_lshl_add_u64 v[206:207], v[206:207], 0, s[24:25]
	s_mov_b32 m0, s26
	global_load_lds_dwordx4 v[206:207], off
	v_lshl_add_u64 v[206:207], v[208:209], 0, s[24:25]
	s_add_i32 m0, s26, 0x2000
	s_add_i32 s26, s31, s8
	global_load_lds_dwordx4 v[206:207], off
	v_lshl_add_u64 v[206:207], v[210:211], 0, s[24:25]
	s_mov_b32 m0, s26
	s_nop 0
	global_load_lds_dwordx4 v[206:207], off
	v_lshl_add_u64 v[206:207], v[212:213], 0, s[24:25]
	s_add_i32 m0, s26, 0x2000
	s_nop 0
	global_load_lds_dwordx4 v[206:207], off
	v_lshl_add_u64 v[206:207], v[214:215], 0, s[24:25]
	s_mov_b32 m0, s59
	s_nop 0
	global_load_lds_dwordx4 v[206:207], off
	v_lshl_add_u64 v[206:207], v[216:217], 0, s[24:25]
	s_mov_b32 m0, s60
	s_nop 0
	global_load_lds_dwordx4 v[206:207], off
	s_waitcnt vmcnt(8)
	s_waitcnt lgkmcnt(0)
	s_barrier
	s_setprio 1
	s_waitcnt lgkmcnt(0)
	v_mfma_f32_16x16x32_bf16 v[64:67], v[138:141], v[174:177], v[64:67]
	v_mfma_f32_16x16x32_bf16 v[60:63], v[150:153], v[174:177], v[60:63]
	v_mfma_f32_16x16x32_bf16 v[48:51], v[138:141], v[182:185], v[48:51]
	v_mfma_f32_16x16x32_bf16 v[44:47], v[150:153], v[182:185], v[44:47]
	v_mfma_f32_16x16x32_bf16 v[32:35], v[138:141], v[190:193], v[32:35]
	v_mfma_f32_16x16x32_bf16 v[28:31], v[150:153], v[190:193], v[28:31]
	v_mfma_f32_16x16x32_bf16 v[16:19], v[138:141], v[198:201], v[16:19]
	v_mfma_f32_16x16x32_bf16 v[12:15], v[150:153], v[198:201], v[12:15]
	v_mfma_f32_16x16x32_bf16 v[64:67], v[146:149], v[178:181], v[64:67]
	v_mfma_f32_16x16x32_bf16 v[60:63], v[154:157], v[178:181], v[60:63]
	v_mfma_f32_16x16x32_bf16 v[48:51], v[146:149], v[186:189], v[48:51]
	v_mfma_f32_16x16x32_bf16 v[44:47], v[154:157], v[186:189], v[44:47]
	v_mfma_f32_16x16x32_bf16 v[32:35], v[146:149], v[194:197], v[32:35]
	v_mfma_f32_16x16x32_bf16 v[28:31], v[154:157], v[194:197], v[28:31]
	v_mfma_f32_16x16x32_bf16 v[16:19], v[146:149], v[202:205], v[16:19]
	v_mfma_f32_16x16x32_bf16 v[12:15], v[154:157], v[202:205], v[12:15]
	s_setprio 0
	s_setprio 1
	v_mfma_f32_16x16x32_bf16 v[56:59], v[158:161], v[174:177], v[56:59]
	v_mfma_f32_16x16x32_bf16 v[52:55], v[166:169], v[174:177], v[52:55]
	v_mfma_f32_16x16x32_bf16 v[40:43], v[158:161], v[182:185], v[40:43]
	v_mfma_f32_16x16x32_bf16 v[36:39], v[166:169], v[182:185], v[36:39]
	v_mfma_f32_16x16x32_bf16 v[24:27], v[158:161], v[190:193], v[24:27]
	v_mfma_f32_16x16x32_bf16 v[20:23], v[166:169], v[190:193], v[20:23]
	v_mfma_f32_16x16x32_bf16 v[8:11], v[158:161], v[198:201], v[8:11]
	v_mfma_f32_16x16x32_bf16 v[4:7], v[166:169], v[198:201], v[4:7]
	v_mfma_f32_16x16x32_bf16 v[56:59], v[162:165], v[178:181], v[56:59]
	v_mfma_f32_16x16x32_bf16 v[52:55], v[170:173], v[178:181], v[52:55]
	v_mfma_f32_16x16x32_bf16 v[40:43], v[162:165], v[186:189], v[40:43]
	v_mfma_f32_16x16x32_bf16 v[36:39], v[170:173], v[186:189], v[36:39]
	v_mfma_f32_16x16x32_bf16 v[24:27], v[162:165], v[194:197], v[24:27]
	v_mfma_f32_16x16x32_bf16 v[20:23], v[170:173], v[194:197], v[20:23]
	v_mfma_f32_16x16x32_bf16 v[8:11], v[162:165], v[202:205], v[8:11]
	v_mfma_f32_16x16x32_bf16 v[4:7], v[170:173], v[202:205], v[4:7]
	s_setprio 0
	s_barrier
	s_add_u32 s42, s42, 0x100
	s_addc_u32 s43, s43, 0
	s_cmp_ge_i32 s19, s57
	s_cbranch_scc0 .LBB0_1033
	s_and_b64 vcc, exec, s[16:17]
	s_cbranch_vccz .LBB0_1036

.LBB0_1276:
	v_add_u32_e32 v85, 0x10000, v250
	ds_read_b128 v[86:89], v85
	ds_read_b128 v[90:93], v85 offset:1024
	ds_read_b128 v[94:97], v85 offset:2048
	ds_read_b128 v[148:151], v85 offset:3072
	v_add_u32_e32 v85, 0x14000, v250
	ds_read_b128 v[152:155], v85
	ds_read_b128 v[156:159], v85 offset:1024
	ds_read_b128 v[160:163], v85 offset:2048
	ds_read_b128 v[164:167], v85 offset:3072
	ds_read_b128 v[168:171], v252
	ds_read_b128 v[172:175], v252 offset:1024
	ds_read_b128 v[176:179], v252 offset:2048
	ds_read_b128 v[180:183], v252 offset:3072
	ds_read_b128 v[184:187], v252 offset:4096
	ds_read_b128 v[188:191], v252 offset:5120
	ds_read_b128 v[192:195], v252 offset:6144
	ds_read_b128 v[202:205], v252 offset:7168
	s_add_u32 s17, s42, 0xfffc0080
	s_addc_u32 s21, s43, -1
	s_cmp_eq_u32 s42, 0x40780
	s_cselect_b64 s[26:27], -1, 0
	s_and_b64 s[34:35], s[26:27], exec
	s_cselect_b32 s21, 0, s21
	s_cselect_b32 s17, 0, s17
	s_and_b64 s[26:27], s[26:27], s[36:37]
	s_and_b64 s[34:35], s[26:27], exec
	s_cselect_b32 s33, s40, s38
	s_cselect_b32 s28, s41, s39
	s_add_u32 s44, s33, s17
	s_addc_u32 s45, s28, s21
	s_add_i32 s28, 0, 0x10000
	s_and_b64 s[26:27], s[26:27], exec
	s_cselect_b32 s33, s31, s1
	s_cselect_b32 s34, s30, s0
	s_add_i32 s35, 0, 0x14000
	s_add_i32 m0, s56, 0xc000
	s_add_u32 s26, s0, s42
	s_addc_u32 s27, s1, s43
	global_load_lds_dwordx4 v2, s[26:27]
	s_add_i32 m0, s56, 0xe000
	v_mov_b32_e32 v199, v3
	global_load_lds_dwordx4 v198, s[26:27]
	s_waitcnt vmcnt(8)
	s_waitcnt lgkmcnt(0)
	s_barrier
	s_setprio 1
	s_waitcnt lgkmcnt(0)
	v_mfma_f32_16x16x32_bf16 v[144:147], v[86:89], v[168:171], v[144:147]
	v_mfma_f32_16x16x32_bf16 v[140:143], v[94:97], v[168:171], v[140:143]
	v_mfma_f32_16x16x32_bf16 v[136:139], v[86:89], v[176:179], v[136:139]
	v_mfma_f32_16x16x32_bf16 v[132:135], v[94:97], v[176:179], v[132:135]
	v_mfma_f32_16x16x32_bf16 v[128:131], v[86:89], v[184:187], v[128:131]
	v_mfma_f32_16x16x32_bf16 v[124:127], v[94:97], v[184:187], v[124:127]
	v_mfma_f32_16x16x32_bf16 v[120:123], v[86:89], v[192:195], v[120:123]
	v_mfma_f32_16x16x32_bf16 v[116:119], v[94:97], v[192:195], v[116:119]
	v_mfma_f32_16x16x32_bf16 v[144:147], v[90:93], v[172:175], v[144:147]
	v_mfma_f32_16x16x32_bf16 v[140:143], v[148:151], v[172:175], v[140:143]
	v_mfma_f32_16x16x32_bf16 v[136:139], v[90:93], v[180:183], v[136:139]
	v_mfma_f32_16x16x32_bf16 v[132:135], v[148:151], v[180:183], v[132:135]
	v_mfma_f32_16x16x32_bf16 v[128:131], v[90:93], v[188:191], v[128:131]
	v_mfma_f32_16x16x32_bf16 v[124:127], v[148:151], v[188:191], v[124:127]
	v_mfma_f32_16x16x32_bf16 v[120:123], v[90:93], v[202:205], v[120:123]
	v_mfma_f32_16x16x32_bf16 v[116:119], v[148:151], v[202:205], v[116:119]
	s_setprio 0
	s_setprio 1
	v_mfma_f32_16x16x32_bf16 v[64:67], v[152:155], v[168:171], v[64:67]
	v_mfma_f32_16x16x32_bf16 v[60:63], v[160:163], v[168:171], v[60:63]
	v_mfma_f32_16x16x32_bf16 v[56:59], v[152:155], v[176:179], v[56:59]
	v_mfma_f32_16x16x32_bf16 v[52:55], v[160:163], v[176:179], v[52:55]
	v_mfma_f32_16x16x32_bf16 v[48:51], v[152:155], v[184:187], v[48:51]
	v_mfma_f32_16x16x32_bf16 v[44:47], v[160:163], v[184:187], v[44:47]
	v_mfma_f32_16x16x32_bf16 v[40:43], v[152:155], v[192:195], v[40:43]
	v_mfma_f32_16x16x32_bf16 v[36:39], v[160:163], v[192:195], v[36:39]
	v_mfma_f32_16x16x32_bf16 v[64:67], v[156:159], v[172:175], v[64:67]
	v_mfma_f32_16x16x32_bf16 v[60:63], v[164:167], v[172:175], v[60:63]
	v_mfma_f32_16x16x32_bf16 v[56:59], v[156:159], v[180:183], v[56:59]
	v_mfma_f32_16x16x32_bf16 v[52:55], v[164:167], v[180:183], v[52:55]
	v_mfma_f32_16x16x32_bf16 v[48:51], v[156:159], v[188:191], v[48:51]
	v_mfma_f32_16x16x32_bf16 v[44:47], v[164:167], v[188:191], v[44:47]
	v_mfma_f32_16x16x32_bf16 v[40:43], v[156:159], v[202:205], v[40:43]
	v_mfma_f32_16x16x32_bf16 v[36:39], v[164:167], v[202:205], v[36:39]
	s_setprio 0
	s_barrier
	ds_read_b128 v[168:171], v252 offset:16384
	ds_read_b128 v[172:175], v252 offset:17408
	ds_read_b128 v[176:179], v252 offset:18432
	ds_read_b128 v[180:183], v252 offset:19456
	ds_read_b128 v[184:187], v252 offset:20480
	ds_read_b128 v[188:191], v252 offset:21504
	ds_read_b128 v[192:195], v252 offset:22528
	ds_read_b128 v[202:205], v252 offset:23552
	s_add_i32 s26, s28, s23
	s_mov_b32 m0, s26
	global_load_lds_dwordx4 v196, s[44:45]
	s_add_i32 m0, s26, 0x2000
	s_add_u32 s26, s44, 0x40000
	s_addc_u32 s27, s45, 0
	s_add_i32 s28, s35, s23
	global_load_lds_dwordx4 v200, s[44:45]
	s_mov_b32 m0, s28
	v_mov_b32_e32 v197, v3
	global_load_lds_dwordx4 v196, s[26:27]
	s_add_i32 m0, s28, 0x2000
	v_mov_b32_e32 v201, v3
	global_load_lds_dwordx4 v200, s[26:27]
	s_add_u32 s26, s34, s17
	s_addc_u32 s27, s33, s21
	s_mov_b32 m0, s56
	v_lshl_add_u64 v[206:207], s[44:45], 0, v[196:197]
	global_load_lds_dwordx4 v2, s[26:27]
	s_mov_b32 m0, s57
	v_lshl_add_u64 v[208:209], s[44:45], 0, v[200:201]
	global_load_lds_dwordx4 v198, s[26:27]
	s_waitcnt vmcnt(8)
	s_waitcnt lgkmcnt(0)
	v_lshl_add_u64 v[210:211], s[26:27], 0, v[2:3]
	v_lshl_add_u64 v[212:213], s[26:27], 0, v[198:199]
	s_barrier
	s_setprio 1
	s_waitcnt lgkmcnt(0)
	v_mfma_f32_16x16x32_bf16 v[112:115], v[86:89], v[168:171], v[112:115]
	v_mfma_f32_16x16x32_bf16 v[108:111], v[94:97], v[168:171], v[108:111]
	v_mfma_f32_16x16x32_bf16 v[104:107], v[86:89], v[176:179], v[104:107]
	v_mfma_f32_16x16x32_bf16 v[98:101], v[94:97], v[176:179], v[100:103]
	v_mfma_f32_16x16x32_bf16 v[80:83], v[86:89], v[184:187], v[80:83]
	v_mfma_f32_16x16x32_bf16 v[76:79], v[94:97], v[184:187], v[76:79]
	v_mfma_f32_16x16x32_bf16 v[72:75], v[86:89], v[192:195], v[72:75]
	v_mfma_f32_16x16x32_bf16 v[68:71], v[94:97], v[192:195], v[68:71]
	v_mfma_f32_16x16x32_bf16 v[112:115], v[90:93], v[172:175], v[112:115]
	v_mfma_f32_16x16x32_bf16 v[108:111], v[148:151], v[172:175], v[108:111]
	v_mfma_f32_16x16x32_bf16 v[104:107], v[90:93], v[180:183], v[104:107]
	v_mfma_f32_16x16x32_bf16 v[98:101], v[148:151], v[180:183], v[98:101]
	v_mfma_f32_16x16x32_bf16 v[80:83], v[90:93], v[188:191], v[80:83]
	v_mfma_f32_16x16x32_bf16 v[76:79], v[148:151], v[188:191], v[76:79]
	v_mfma_f32_16x16x32_bf16 v[72:75], v[90:93], v[202:205], v[72:75]
	v_mfma_f32_16x16x32_bf16 v[68:71], v[148:151], v[202:205], v[68:71]
	s_setprio 0
	s_setprio 1
	v_mfma_f32_16x16x32_bf16 v[32:35], v[152:155], v[168:171], v[32:35]
	v_mfma_f32_16x16x32_bf16 v[28:31], v[160:163], v[168:171], v[28:31]
	v_mfma_f32_16x16x32_bf16 v[24:27], v[152:155], v[176:179], v[24:27]
	v_mfma_f32_16x16x32_bf16 v[20:23], v[160:163], v[176:179], v[20:23]
	v_mfma_f32_16x16x32_bf16 v[16:19], v[152:155], v[184:187], v[16:19]
	v_mfma_f32_16x16x32_bf16 v[12:15], v[160:163], v[184:187], v[12:15]
	v_mfma_f32_16x16x32_bf16 v[8:11], v[152:155], v[192:195], v[8:11]
	v_mfma_f32_16x16x32_bf16 v[4:7], v[160:163], v[192:195], v[4:7]
	v_mfma_f32_16x16x32_bf16 v[32:35], v[156:159], v[172:175], v[32:35]
	v_mfma_f32_16x16x32_bf16 v[28:31], v[164:167], v[172:175], v[28:31]
	v_mfma_f32_16x16x32_bf16 v[24:27], v[156:159], v[180:183], v[24:27]
	v_mfma_f32_16x16x32_bf16 v[20:23], v[164:167], v[180:183], v[20:23]
	v_mfma_f32_16x16x32_bf16 v[16:19], v[156:159], v[188:191], v[16:19]
	v_mfma_f32_16x16x32_bf16 v[12:15], v[164:167], v[188:191], v[12:15]
	v_mfma_f32_16x16x32_bf16 v[8:11], v[156:159], v[202:205], v[8:11]
	v_mfma_f32_16x16x32_bf16 v[4:7], v[164:167], v[202:205], v[4:7]
	s_setprio 0
	s_barrier
	v_add_u32_e32 v85, 0x18000, v250
	ds_read_b128 v[86:89], v85
	ds_read_b128 v[90:93], v85 offset:1024
	ds_read_b128 v[94:97], v85 offset:2048
	ds_read_b128 v[148:151], v85 offset:3072
	v_add_u32_e32 v85, 0x1c000, v250
	ds_read_b128 v[152:155], v85
	ds_read_b128 v[156:159], v85 offset:1024
	ds_read_b128 v[160:163], v85 offset:2048
	ds_read_b128 v[164:167], v85 offset:3072
	ds_read_b128 v[168:171], v252 offset:32768
	ds_read_b128 v[172:175], v252 offset:33792
	ds_read_b128 v[176:179], v252 offset:34816
	ds_read_b128 v[180:183], v252 offset:35840
	ds_read_b128 v[184:187], v252 offset:36864
	ds_read_b128 v[188:191], v252 offset:37888
	ds_read_b128 v[192:195], v252 offset:38912
	ds_read_b128 v[202:205], v252 offset:39936
	s_add_i32 s17, 0, 0x18000
	s_add_i32 s21, 0, 0x1c000
	s_add_u32 s26, s26, 0x40000
	s_addc_u32 s27, s27, 0
	s_mov_b32 m0, s58
	global_load_lds_dwordx4 v2, s[26:27]
	s_mov_b32 m0, s59
	s_nop 0
	global_load_lds_dwordx4 v198, s[26:27]
	s_waitcnt vmcnt(8)
	s_waitcnt lgkmcnt(0)
	s_barrier
	s_setprio 1
	s_waitcnt lgkmcnt(0)
	v_mfma_f32_16x16x32_bf16 v[144:147], v[86:89], v[168:171], v[144:147]
	v_mfma_f32_16x16x32_bf16 v[140:143], v[94:97], v[168:171], v[140:143]
	v_mfma_f32_16x16x32_bf16 v[136:139], v[86:89], v[176:179], v[136:139]
	v_mfma_f32_16x16x32_bf16 v[132:135], v[94:97], v[176:179], v[132:135]
	v_mfma_f32_16x16x32_bf16 v[128:131], v[86:89], v[184:187], v[128:131]
	v_mfma_f32_16x16x32_bf16 v[124:127], v[94:97], v[184:187], v[124:127]
	v_mfma_f32_16x16x32_bf16 v[120:123], v[86:89], v[192:195], v[120:123]
	v_mfma_f32_16x16x32_bf16 v[116:119], v[94:97], v[192:195], v[116:119]
	v_mfma_f32_16x16x32_bf16 v[144:147], v[90:93], v[172:175], v[144:147]
	v_mfma_f32_16x16x32_bf16 v[140:143], v[148:151], v[172:175], v[140:143]
	v_mfma_f32_16x16x32_bf16 v[136:139], v[90:93], v[180:183], v[136:139]
	v_mfma_f32_16x16x32_bf16 v[132:135], v[148:151], v[180:183], v[132:135]
	v_mfma_f32_16x16x32_bf16 v[128:131], v[90:93], v[188:191], v[128:131]
	v_mfma_f32_16x16x32_bf16 v[124:127], v[148:151], v[188:191], v[124:127]
	v_mfma_f32_16x16x32_bf16 v[120:123], v[90:93], v[202:205], v[120:123]
	v_mfma_f32_16x16x32_bf16 v[116:119], v[148:151], v[202:205], v[116:119]
	s_setprio 0
	s_setprio 1
	v_mfma_f32_16x16x32_bf16 v[64:67], v[152:155], v[168:171], v[64:67]
	v_mfma_f32_16x16x32_bf16 v[60:63], v[160:163], v[168:171], v[60:63]
	v_mfma_f32_16x16x32_bf16 v[56:59], v[152:155], v[176:179], v[56:59]
	v_mfma_f32_16x16x32_bf16 v[52:55], v[160:163], v[176:179], v[52:55]
	v_mfma_f32_16x16x32_bf16 v[48:51], v[152:155], v[184:187], v[48:51]
	v_mfma_f32_16x16x32_bf16 v[44:47], v[160:163], v[184:187], v[44:47]
	v_mfma_f32_16x16x32_bf16 v[40:43], v[152:155], v[192:195], v[40:43]
	v_mfma_f32_16x16x32_bf16 v[36:39], v[160:163], v[192:195], v[36:39]
	v_mfma_f32_16x16x32_bf16 v[64:67], v[156:159], v[172:175], v[64:67]
	v_mfma_f32_16x16x32_bf16 v[60:63], v[164:167], v[172:175], v[60:63]
	v_mfma_f32_16x16x32_bf16 v[56:59], v[156:159], v[180:183], v[56:59]
	v_mfma_f32_16x16x32_bf16 v[52:55], v[164:167], v[180:183], v[52:55]
	v_mfma_f32_16x16x32_bf16 v[48:51], v[156:159], v[188:191], v[48:51]
	v_mfma_f32_16x16x32_bf16 v[44:47], v[164:167], v[188:191], v[44:47]
	v_mfma_f32_16x16x32_bf16 v[40:43], v[156:159], v[202:205], v[40:43]
	v_mfma_f32_16x16x32_bf16 v[36:39], v[164:167], v[202:205], v[36:39]
	s_setprio 0
	s_barrier
	ds_read_b128 v[168:171], v252 offset:49152
	ds_read_b128 v[172:175], v252 offset:50176
	ds_read_b128 v[176:179], v252 offset:51200
	ds_read_b128 v[180:183], v252 offset:52224
	ds_read_b128 v[184:187], v252 offset:53248
	ds_read_b128 v[188:191], v252 offset:54272
	ds_read_b128 v[192:195], v252 offset:55296
	ds_read_b128 v[202:205], v252 offset:56320
	s_add_i32 s17, s17, s23
	v_lshl_add_u64 v[102:103], v[206:207], 0, s[24:25]
	s_mov_b32 m0, s17
	global_load_lds_dwordx4 v[102:103], off
	s_add_i32 m0, s17, 0x2000
	s_add_u32 s26, s44, 0x40080
	v_lshl_add_u64 v[102:103], v[208:209], 0, s[24:25]
	s_addc_u32 s27, s45, 0
	s_add_i32 s17, s21, s23
	global_load_lds_dwordx4 v[102:103], off
	s_mov_b32 m0, s17
	v_lshl_add_u64 v[102:103], v[210:211], 0, s[24:25]
	global_load_lds_dwordx4 v196, s[26:27]
	s_add_i32 m0, s17, 0x2000
	s_nop 0
	global_load_lds_dwordx4 v200, s[26:27]
	s_mov_b32 m0, s61
	s_nop 0
	global_load_lds_dwordx4 v[102:103], off
	v_lshl_add_u64 v[102:103], v[212:213], 0, s[24:25]
	s_mov_b32 m0, s62
	s_nop 0
	global_load_lds_dwordx4 v[102:103], off
	s_waitcnt vmcnt(8)
	s_waitcnt lgkmcnt(0)
	s_barrier
	s_setprio 1
	s_waitcnt lgkmcnt(0)
	v_mfma_f32_16x16x32_bf16 v[112:115], v[86:89], v[168:171], v[112:115]
	v_mfma_f32_16x16x32_bf16 v[108:111], v[94:97], v[168:171], v[108:111]
	v_mfma_f32_16x16x32_bf16 v[102:105], v[86:89], v[176:179], v[104:107]
	v_mfma_f32_16x16x32_bf16 v[98:101], v[94:97], v[176:179], v[98:101]
	v_mfma_f32_16x16x32_bf16 v[80:83], v[86:89], v[184:187], v[80:83]
	v_mfma_f32_16x16x32_bf16 v[76:79], v[94:97], v[184:187], v[76:79]
	v_mfma_f32_16x16x32_bf16 v[72:75], v[86:89], v[192:195], v[72:75]
	v_mfma_f32_16x16x32_bf16 v[68:71], v[94:97], v[192:195], v[68:71]
	v_mfma_f32_16x16x32_bf16 v[112:115], v[90:93], v[172:175], v[112:115]
	v_mfma_f32_16x16x32_bf16 v[108:111], v[148:151], v[172:175], v[108:111]
	v_mfma_f32_16x16x32_bf16 v[104:107], v[90:93], v[180:183], v[102:105]
	v_mfma_f32_16x16x32_bf16 v[100:103], v[148:151], v[180:183], v[98:101]
	v_mfma_f32_16x16x32_bf16 v[80:83], v[90:93], v[188:191], v[80:83]
	v_mfma_f32_16x16x32_bf16 v[76:79], v[148:151], v[188:191], v[76:79]
	v_mfma_f32_16x16x32_bf16 v[72:75], v[90:93], v[202:205], v[72:75]
	v_mfma_f32_16x16x32_bf16 v[68:71], v[148:151], v[202:205], v[68:71]
	s_setprio 0
	s_setprio 1
	v_mfma_f32_16x16x32_bf16 v[32:35], v[152:155], v[168:171], v[32:35]
	v_mfma_f32_16x16x32_bf16 v[28:31], v[160:163], v[168:171], v[28:31]
	v_mfma_f32_16x16x32_bf16 v[24:27], v[152:155], v[176:179], v[24:27]
	v_mfma_f32_16x16x32_bf16 v[20:23], v[160:163], v[176:179], v[20:23]
	v_mfma_f32_16x16x32_bf16 v[16:19], v[152:155], v[184:187], v[16:19]
	v_mfma_f32_16x16x32_bf16 v[12:15], v[160:163], v[184:187], v[12:15]
	v_mfma_f32_16x16x32_bf16 v[8:11], v[152:155], v[192:195], v[8:11]
	v_mfma_f32_16x16x32_bf16 v[4:7], v[160:163], v[192:195], v[4:7]
	v_mfma_f32_16x16x32_bf16 v[32:35], v[156:159], v[172:175], v[32:35]
	v_mfma_f32_16x16x32_bf16 v[28:31], v[164:167], v[172:175], v[28:31]
	v_mfma_f32_16x16x32_bf16 v[24:27], v[156:159], v[180:183], v[24:27]
	v_mfma_f32_16x16x32_bf16 v[20:23], v[164:167], v[180:183], v[20:23]
	v_mfma_f32_16x16x32_bf16 v[16:19], v[156:159], v[188:191], v[16:19]
	v_mfma_f32_16x16x32_bf16 v[12:15], v[164:167], v[188:191], v[12:15]
	v_mfma_f32_16x16x32_bf16 v[8:11], v[156:159], v[202:205], v[8:11]
	v_mfma_f32_16x16x32_bf16 v[4:7], v[164:167], v[202:205], v[4:7]
	s_setprio 0
	s_barrier
	s_cmp_lg_u32 s42, 0x40380
	s_cbranch_scc1 .LBB0_1275
; __device__ __forceinline__ LAS float* T1(ldsp tab, int par) { return (LAS float*)(tab + 2048) + par * 256; }
;     __device__ __forceinline__ void midscale(Acc& acc, int par, ldsp tab, int wr, int fr) const {
; #pragma unroll
;         for (int ai = 0; ai < 2; ++ai)
; #pragma unroll
;             for (int m = 0; m < 4; ++m) { const float f = T1(tab, par)[ai * 128 + wr * 64 + m * 16 + fr];
; #pragma unroll
;                 for (int bj = 0; bj < 2; ++bj)
; #pragma unroll
;                     for (int n = 0; n < 2; ++n) acc[ai][bj][m][n] = acc[ai][bj][m][n] * f; } }
	ds_read2_b32 v[86:87], v84 offset1:16
	s_waitcnt lgkmcnt(0)
	v_pk_mul_f32 v[146:147], v[146:147], v[86:87] op_sel_hi:[1,0]
	v_pk_mul_f32 v[144:145], v[144:145], v[86:87] op_sel_hi:[1,0]
	v_pk_mul_f32 v[142:143], v[142:143], v[86:87] op_sel_hi:[1,0]
	v_pk_mul_f32 v[140:141], v[140:141], v[86:87] op_sel_hi:[1,0]
	v_pk_mul_f32 v[66:67], v[66:67], v[86:87] op_sel_hi:[1,0]
	v_pk_mul_f32 v[64:65], v[64:65], v[86:87] op_sel_hi:[1,0]
	v_pk_mul_f32 v[62:63], v[62:63], v[86:87] op_sel_hi:[1,0]
	v_pk_mul_f32 v[60:61], v[60:61], v[86:87] op_sel_hi:[1,0]
	v_mov_b32_e32 v86, v87
	v_pk_mul_f32 v[138:139], v[138:139], v[86:87] op_sel_hi:[1,0]
	v_pk_mul_f32 v[136:137], v[136:137], v[86:87] op_sel_hi:[1,0]
	v_pk_mul_f32 v[134:135], v[134:135], v[86:87] op_sel_hi:[1,0]
	v_pk_mul_f32 v[132:133], v[132:133], v[86:87] op_sel_hi:[1,0]
	v_pk_mul_f32 v[58:59], v[58:59], v[86:87] op_sel_hi:[1,0]
	v_pk_mul_f32 v[56:57], v[56:57], v[86:87] op_sel_hi:[1,0]
	v_pk_mul_f32 v[54:55], v[54:55], v[86:87] op_sel_hi:[1,0]
	v_pk_mul_f32 v[52:53], v[52:53], v[86:87] op_sel_hi:[1,0]
	ds_read2_b32 v[86:87], v84 offset0:32 offset1:48
	s_waitcnt lgkmcnt(0)
	v_pk_mul_f32 v[130:131], v[130:131], v[86:87] op_sel_hi:[1,0]
	v_pk_mul_f32 v[128:129], v[128:129], v[86:87] op_sel_hi:[1,0]
	v_pk_mul_f32 v[126:127], v[126:127], v[86:87] op_sel_hi:[1,0]
	v_pk_mul_f32 v[124:125], v[124:125], v[86:87] op_sel_hi:[1,0]
	v_pk_mul_f32 v[50:51], v[50:51], v[86:87] op_sel_hi:[1,0]
	v_pk_mul_f32 v[48:49], v[48:49], v[86:87] op_sel_hi:[1,0]
	v_pk_mul_f32 v[46:47], v[46:47], v[86:87] op_sel_hi:[1,0]
	v_pk_mul_f32 v[44:45], v[44:45], v[86:87] op_sel_hi:[1,0]
	v_mov_b32_e32 v86, v87
	v_pk_mul_f32 v[122:123], v[122:123], v[86:87] op_sel_hi:[1,0]
	v_pk_mul_f32 v[120:121], v[120:121], v[86:87] op_sel_hi:[1,0]
	v_pk_mul_f32 v[118:119], v[118:119], v[86:87] op_sel_hi:[1,0]
	v_pk_mul_f32 v[116:117], v[116:117], v[86:87] op_sel_hi:[1,0]
	v_pk_mul_f32 v[42:43], v[42:43], v[86:87] op_sel_hi:[1,0]
	v_pk_mul_f32 v[40:41], v[40:41], v[86:87] op_sel_hi:[1,0]
	v_pk_mul_f32 v[38:39], v[38:39], v[86:87] op_sel_hi:[1,0]
	v_pk_mul_f32 v[36:37], v[36:37], v[86:87] op_sel_hi:[1,0]
	ds_read2_b32 v[86:87], v84 offset0:128 offset1:144
	s_waitcnt lgkmcnt(0)
	v_pk_mul_f32 v[114:115], v[114:115], v[86:87] op_sel_hi:[1,0]
	v_pk_mul_f32 v[112:113], v[112:113], v[86:87] op_sel_hi:[1,0]
	v_pk_mul_f32 v[110:111], v[110:111], v[86:87] op_sel_hi:[1,0]
	v_pk_mul_f32 v[108:109], v[108:109], v[86:87] op_sel_hi:[1,0]
	v_pk_mul_f32 v[34:35], v[34:35], v[86:87] op_sel_hi:[1,0]
	v_pk_mul_f32 v[32:33], v[32:33], v[86:87] op_sel_hi:[1,0]
	v_pk_mul_f32 v[30:31], v[30:31], v[86:87] op_sel_hi:[1,0]
	v_pk_mul_f32 v[28:29], v[28:29], v[86:87] op_sel_hi:[1,0]
	v_mov_b32_e32 v86, v87
	v_pk_mul_f32 v[106:107], v[106:107], v[86:87] op_sel_hi:[1,0]
	v_pk_mul_f32 v[104:105], v[104:105], v[86:87] op_sel_hi:[1,0]
	v_pk_mul_f32 v[102:103], v[102:103], v[86:87] op_sel_hi:[1,0]
	v_pk_mul_f32 v[100:101], v[100:101], v[86:87] op_sel_hi:[1,0]
	v_pk_mul_f32 v[26:27], v[26:27], v[86:87] op_sel_hi:[1,0]
	v_pk_mul_f32 v[24:25], v[24:25], v[86:87] op_sel_hi:[1,0]
	v_pk_mul_f32 v[22:23], v[22:23], v[86:87] op_sel_hi:[1,0]
	v_pk_mul_f32 v[20:21], v[20:21], v[86:87] op_sel_hi:[1,0]
	ds_read2_b32 v[86:87], v84 offset0:160 offset1:176
	s_waitcnt lgkmcnt(0)
	v_pk_mul_f32 v[82:83], v[82:83], v[86:87] op_sel_hi:[1,0]
	v_pk_mul_f32 v[80:81], v[80:81], v[86:87] op_sel_hi:[1,0]
	v_pk_mul_f32 v[78:79], v[78:79], v[86:87] op_sel_hi:[1,0]
	v_pk_mul_f32 v[76:77], v[76:77], v[86:87] op_sel_hi:[1,0]
	v_pk_mul_f32 v[18:19], v[18:19], v[86:87] op_sel_hi:[1,0]
	v_pk_mul_f32 v[16:17], v[16:17], v[86:87] op_sel_hi:[1,0]
	v_pk_mul_f32 v[14:15], v[14:15], v[86:87] op_sel_hi:[1,0]
	v_pk_mul_f32 v[12:13], v[12:13], v[86:87] op_sel_hi:[1,0]
	v_mov_b32_e32 v86, v87
	v_pk_mul_f32 v[74:75], v[74:75], v[86:87] op_sel_hi:[1,0]
	v_pk_mul_f32 v[72:73], v[72:73], v[86:87] op_sel_hi:[1,0]
	v_pk_mul_f32 v[70:71], v[70:71], v[86:87] op_sel_hi:[1,0]
	v_pk_mul_f32 v[68:69], v[68:69], v[86:87] op_sel_hi:[1,0]
	v_pk_mul_f32 v[10:11], v[10:11], v[86:87] op_sel_hi:[1,0]
	v_pk_mul_f32 v[8:9], v[8:9], v[86:87] op_sel_hi:[1,0]
	v_pk_mul_f32 v[6:7], v[6:7], v[86:87] op_sel_hi:[1,0]
	v_pk_mul_f32 v[4:5], v[4:5], v[86:87] op_sel_hi:[1,0]
	s_branch .LBB0_1275

.LBB0_1920:
	v_add_u32_e32 v144, 0x10000, v159
	v_add_u32_e32 v149, 0x14000, v159
	ds_read_b128 v[132:135], v144
	ds_read_b128 v[136:139], v144 offset:1024
	ds_read_b128 v[140:143], v144 offset:2048
	ds_read_b128 v[144:147], v144 offset:3072
	ds_read_b128 v[154:157], v149
	ds_read_b128 v[162:165], v149 offset:1024
	ds_read_b128 v[166:169], v149 offset:2048
	ds_read_b128 v[170:173], v149 offset:3072
	ds_read_b128 v[174:177], v160
	ds_read_b128 v[178:181], v160 offset:1024
	ds_read_b128 v[182:185], v160 offset:2048
	ds_read_b128 v[186:189], v160 offset:3072
	ds_read_b128 v[190:193], v160 offset:4096
	ds_read_b128 v[194:197], v160 offset:5120
	ds_read_b128 v[198:201], v160 offset:6144
	ds_read_b128 v[202:205], v160 offset:7168
	s_add_u32 s15, s30, 0xfffc0080
	s_addc_u32 s21, s31, -1
	s_cmp_eq_u32 s13, 12
	s_cselect_b64 s[26:27], -1, 0
	s_and_b64 s[34:35], s[26:27], exec
	s_cselect_b32 s21, 0, s21
	s_cselect_b32 s15, 0, s15
	s_and_b64 s[26:27], s[26:27], s[36:37]
	s_and_b64 s[34:35], s[26:27], exec
	s_cselect_b32 s33, s18, s22
	s_cselect_b32 s28, s19, s23
	s_add_u32 s38, s33, s15
	s_addc_u32 s39, s28, s21
	s_add_i32 s28, 0, 0x10000
	s_and_b64 s[26:27], s[26:27], exec
	s_cselect_b32 s33, s17, s1
	s_cselect_b32 s34, s16, s0
	s_add_i32 s35, 0, 0x14000
	s_add_i32 m0, s48, 0xc000
	s_add_u32 s26, s0, s30
	s_addc_u32 s27, s1, s31
	global_load_lds_dwordx4 v2, s[26:27]
	s_add_i32 m0, s48, 0xe000
	v_mov_b32_e32 v151, v3
	global_load_lds_dwordx4 v150, s[26:27]
	s_waitcnt vmcnt(8)
	s_waitcnt lgkmcnt(0)
	s_barrier
	s_setprio 1
	s_waitcnt lgkmcnt(0)
	v_mfma_f32_16x16x32_bf16 v[128:131], v[132:135], v[174:177], v[128:131]
	v_mfma_f32_16x16x32_bf16 v[124:127], v[140:143], v[174:177], v[124:127]
	v_mfma_f32_16x16x32_bf16 v[112:115], v[132:135], v[182:185], v[112:115]
	v_mfma_f32_16x16x32_bf16 v[108:111], v[140:143], v[182:185], v[108:111]
	v_mfma_f32_16x16x32_bf16 v[96:99], v[132:135], v[190:193], v[96:99]
	v_mfma_f32_16x16x32_bf16 v[92:95], v[140:143], v[190:193], v[92:95]
	v_mfma_f32_16x16x32_bf16 v[80:83], v[132:135], v[198:201], v[80:83]
	v_mfma_f32_16x16x32_bf16 v[76:79], v[140:143], v[198:201], v[76:79]
	v_mfma_f32_16x16x32_bf16 v[128:131], v[136:139], v[178:181], v[128:131]
	v_mfma_f32_16x16x32_bf16 v[124:127], v[144:147], v[178:181], v[124:127]
	v_mfma_f32_16x16x32_bf16 v[112:115], v[136:139], v[186:189], v[112:115]
	v_mfma_f32_16x16x32_bf16 v[108:111], v[144:147], v[186:189], v[108:111]
	v_mfma_f32_16x16x32_bf16 v[96:99], v[136:139], v[194:197], v[96:99]
	v_mfma_f32_16x16x32_bf16 v[92:95], v[144:147], v[194:197], v[92:95]
	v_mfma_f32_16x16x32_bf16 v[80:83], v[136:139], v[202:205], v[80:83]
	v_mfma_f32_16x16x32_bf16 v[76:79], v[144:147], v[202:205], v[76:79]
	s_setprio 0
	s_setprio 1
	v_mfma_f32_16x16x32_bf16 v[120:123], v[154:157], v[174:177], v[120:123]
	v_mfma_f32_16x16x32_bf16 v[116:119], v[166:169], v[174:177], v[116:119]
	v_mfma_f32_16x16x32_bf16 v[104:107], v[154:157], v[182:185], v[104:107]
	v_mfma_f32_16x16x32_bf16 v[100:103], v[166:169], v[182:185], v[100:103]
	v_mfma_f32_16x16x32_bf16 v[88:91], v[154:157], v[190:193], v[88:91]
	v_mfma_f32_16x16x32_bf16 v[84:87], v[166:169], v[190:193], v[84:87]
	v_mfma_f32_16x16x32_bf16 v[72:75], v[154:157], v[198:201], v[72:75]
	v_mfma_f32_16x16x32_bf16 v[68:71], v[166:169], v[198:201], v[68:71]
	v_mfma_f32_16x16x32_bf16 v[120:123], v[162:165], v[178:181], v[120:123]
	v_mfma_f32_16x16x32_bf16 v[116:119], v[170:173], v[178:181], v[116:119]
	v_mfma_f32_16x16x32_bf16 v[104:107], v[162:165], v[186:189], v[104:107]
	v_mfma_f32_16x16x32_bf16 v[100:103], v[170:173], v[186:189], v[100:103]
	v_mfma_f32_16x16x32_bf16 v[88:91], v[162:165], v[194:197], v[88:91]
	v_mfma_f32_16x16x32_bf16 v[84:87], v[170:173], v[194:197], v[84:87]
	v_mfma_f32_16x16x32_bf16 v[72:75], v[162:165], v[202:205], v[72:75]
	v_mfma_f32_16x16x32_bf16 v[68:71], v[170:173], v[202:205], v[68:71]
	s_setprio 0
	s_barrier
	ds_read_b128 v[174:177], v160 offset:16384
	ds_read_b128 v[178:181], v160 offset:17408
	ds_read_b128 v[182:185], v160 offset:18432
	ds_read_b128 v[186:189], v160 offset:19456
	ds_read_b128 v[190:193], v160 offset:20480
	ds_read_b128 v[194:197], v160 offset:21504
	ds_read_b128 v[198:201], v160 offset:22528
	ds_read_b128 v[202:205], v160 offset:23552
	s_add_i32 s26, s28, s45
	s_mov_b32 m0, s26
	global_load_lds_dwordx4 v148, s[38:39]
	s_add_i32 m0, s26, 0x2000
	s_add_u32 s26, s38, 0x40000
	s_addc_u32 s27, s39, 0
	s_add_i32 s28, s35, s45
	global_load_lds_dwordx4 v152, s[38:39]
	s_mov_b32 m0, s28
	v_mov_b32_e32 v149, v3
	global_load_lds_dwordx4 v148, s[26:27]
	s_add_i32 m0, s28, 0x2000
	v_mov_b32_e32 v153, v3
	global_load_lds_dwordx4 v152, s[26:27]
	s_add_u32 s26, s34, s15
	s_addc_u32 s27, s33, s21
	s_mov_b32 m0, s48
	v_lshl_add_u64 v[206:207], s[38:39], 0, v[148:149]
	global_load_lds_dwordx4 v2, s[26:27]
	s_mov_b32 m0, s49
	v_lshl_add_u64 v[208:209], s[38:39], 0, v[152:153]
	global_load_lds_dwordx4 v150, s[26:27]
	s_waitcnt vmcnt(8)
	s_waitcnt lgkmcnt(0)
	v_lshl_add_u64 v[210:211], s[26:27], 0, v[2:3]
	v_lshl_add_u64 v[212:213], s[26:27], 0, v[150:151]
	s_barrier
	s_setprio 1
	s_waitcnt lgkmcnt(0)
	v_mfma_f32_16x16x32_bf16 v[64:67], v[132:135], v[174:177], v[64:67]
	v_mfma_f32_16x16x32_bf16 v[60:63], v[140:143], v[174:177], v[60:63]
	v_mfma_f32_16x16x32_bf16 v[48:51], v[132:135], v[182:185], v[48:51]
	v_mfma_f32_16x16x32_bf16 v[44:47], v[140:143], v[182:185], v[44:47]
	v_mfma_f32_16x16x32_bf16 v[32:35], v[132:135], v[190:193], v[32:35]
	v_mfma_f32_16x16x32_bf16 v[28:31], v[140:143], v[190:193], v[28:31]
	v_mfma_f32_16x16x32_bf16 v[16:19], v[132:135], v[198:201], v[16:19]
	v_mfma_f32_16x16x32_bf16 v[12:15], v[140:143], v[198:201], v[12:15]
	v_mfma_f32_16x16x32_bf16 v[64:67], v[136:139], v[178:181], v[64:67]
	v_mfma_f32_16x16x32_bf16 v[60:63], v[144:147], v[178:181], v[60:63]
	v_mfma_f32_16x16x32_bf16 v[48:51], v[136:139], v[186:189], v[48:51]
	v_mfma_f32_16x16x32_bf16 v[44:47], v[144:147], v[186:189], v[44:47]
	v_mfma_f32_16x16x32_bf16 v[32:35], v[136:139], v[194:197], v[32:35]
	v_mfma_f32_16x16x32_bf16 v[28:31], v[144:147], v[194:197], v[28:31]
	v_mfma_f32_16x16x32_bf16 v[16:19], v[136:139], v[202:205], v[16:19]
	v_mfma_f32_16x16x32_bf16 v[12:15], v[144:147], v[202:205], v[12:15]
	s_setprio 0
	s_setprio 1
	v_mfma_f32_16x16x32_bf16 v[56:59], v[154:157], v[174:177], v[56:59]
	v_mfma_f32_16x16x32_bf16 v[52:55], v[166:169], v[174:177], v[52:55]
	v_mfma_f32_16x16x32_bf16 v[40:43], v[154:157], v[182:185], v[40:43]
	v_mfma_f32_16x16x32_bf16 v[36:39], v[166:169], v[182:185], v[36:39]
	v_mfma_f32_16x16x32_bf16 v[24:27], v[154:157], v[190:193], v[24:27]
	v_mfma_f32_16x16x32_bf16 v[20:23], v[166:169], v[190:193], v[20:23]
	v_mfma_f32_16x16x32_bf16 v[8:11], v[154:157], v[198:201], v[8:11]
	v_mfma_f32_16x16x32_bf16 v[4:7], v[166:169], v[198:201], v[4:7]
	v_mfma_f32_16x16x32_bf16 v[56:59], v[162:165], v[178:181], v[56:59]
	v_mfma_f32_16x16x32_bf16 v[52:55], v[170:173], v[178:181], v[52:55]
	v_mfma_f32_16x16x32_bf16 v[40:43], v[162:165], v[186:189], v[40:43]
	v_mfma_f32_16x16x32_bf16 v[36:39], v[170:173], v[186:189], v[36:39]
	v_mfma_f32_16x16x32_bf16 v[24:27], v[162:165], v[194:197], v[24:27]
	v_mfma_f32_16x16x32_bf16 v[20:23], v[170:173], v[194:197], v[20:23]
	v_mfma_f32_16x16x32_bf16 v[8:11], v[162:165], v[202:205], v[8:11]
	v_mfma_f32_16x16x32_bf16 v[4:7], v[170:173], v[202:205], v[4:7]
	s_setprio 0
	s_barrier
	v_add_u32_e32 v144, 0x18000, v159
	v_add_u32_e32 v149, 0x1c000, v159
	ds_read_b128 v[132:135], v144
	ds_read_b128 v[136:139], v144 offset:1024
	ds_read_b128 v[140:143], v144 offset:2048
	ds_read_b128 v[144:147], v144 offset:3072
	ds_read_b128 v[154:157], v149
	ds_read_b128 v[162:165], v149 offset:1024
	ds_read_b128 v[166:169], v149 offset:2048
	ds_read_b128 v[170:173], v149 offset:3072
	ds_read_b128 v[174:177], v160 offset:32768
	ds_read_b128 v[178:181], v160 offset:33792
	ds_read_b128 v[182:185], v160 offset:34816
	ds_read_b128 v[186:189], v160 offset:35840
	ds_read_b128 v[190:193], v160 offset:36864
	ds_read_b128 v[194:197], v160 offset:37888
	ds_read_b128 v[198:201], v160 offset:38912
	ds_read_b128 v[202:205], v160 offset:39936
	s_add_i32 s15, 0, 0x18000
	s_add_i32 s21, 0, 0x1c000
	s_add_u32 s26, s26, 0x40000
	s_addc_u32 s27, s27, 0
	s_mov_b32 m0, s50
	global_load_lds_dwordx4 v2, s[26:27]
	s_mov_b32 m0, s51
	s_nop 0
	global_load_lds_dwordx4 v150, s[26:27]
	s_waitcnt vmcnt(8)
	s_waitcnt lgkmcnt(0)
	s_barrier
	s_setprio 1
	s_waitcnt lgkmcnt(0)
	v_mfma_f32_16x16x32_bf16 v[128:131], v[132:135], v[174:177], v[128:131]
	v_mfma_f32_16x16x32_bf16 v[124:127], v[140:143], v[174:177], v[124:127]
	v_mfma_f32_16x16x32_bf16 v[112:115], v[132:135], v[182:185], v[112:115]
	v_mfma_f32_16x16x32_bf16 v[108:111], v[140:143], v[182:185], v[108:111]
	v_mfma_f32_16x16x32_bf16 v[96:99], v[132:135], v[190:193], v[96:99]
	v_mfma_f32_16x16x32_bf16 v[92:95], v[140:143], v[190:193], v[92:95]
	v_mfma_f32_16x16x32_bf16 v[80:83], v[132:135], v[198:201], v[80:83]
	v_mfma_f32_16x16x32_bf16 v[76:79], v[140:143], v[198:201], v[76:79]
	v_mfma_f32_16x16x32_bf16 v[128:131], v[136:139], v[178:181], v[128:131]
	v_mfma_f32_16x16x32_bf16 v[124:127], v[144:147], v[178:181], v[124:127]
	v_mfma_f32_16x16x32_bf16 v[112:115], v[136:139], v[186:189], v[112:115]
	v_mfma_f32_16x16x32_bf16 v[108:111], v[144:147], v[186:189], v[108:111]
	v_mfma_f32_16x16x32_bf16 v[96:99], v[136:139], v[194:197], v[96:99]
	v_mfma_f32_16x16x32_bf16 v[92:95], v[144:147], v[194:197], v[92:95]
	v_mfma_f32_16x16x32_bf16 v[80:83], v[136:139], v[202:205], v[80:83]
	v_mfma_f32_16x16x32_bf16 v[76:79], v[144:147], v[202:205], v[76:79]
	s_setprio 0
	s_setprio 1
	v_mfma_f32_16x16x32_bf16 v[120:123], v[154:157], v[174:177], v[120:123]
	v_mfma_f32_16x16x32_bf16 v[116:119], v[166:169], v[174:177], v[116:119]
	v_mfma_f32_16x16x32_bf16 v[104:107], v[154:157], v[182:185], v[104:107]
	v_mfma_f32_16x16x32_bf16 v[100:103], v[166:169], v[182:185], v[100:103]
	v_mfma_f32_16x16x32_bf16 v[88:91], v[154:157], v[190:193], v[88:91]
	v_mfma_f32_16x16x32_bf16 v[84:87], v[166:169], v[190:193], v[84:87]
	v_mfma_f32_16x16x32_bf16 v[72:75], v[154:157], v[198:201], v[72:75]
	v_mfma_f32_16x16x32_bf16 v[68:71], v[166:169], v[198:201], v[68:71]
	v_mfma_f32_16x16x32_bf16 v[120:123], v[162:165], v[178:181], v[120:123]
	v_mfma_f32_16x16x32_bf16 v[116:119], v[170:173], v[178:181], v[116:119]
	v_mfma_f32_16x16x32_bf16 v[104:107], v[162:165], v[186:189], v[104:107]
	v_mfma_f32_16x16x32_bf16 v[100:103], v[170:173], v[186:189], v[100:103]
	v_mfma_f32_16x16x32_bf16 v[88:91], v[162:165], v[194:197], v[88:91]
	v_mfma_f32_16x16x32_bf16 v[84:87], v[170:173], v[194:197], v[84:87]
	v_mfma_f32_16x16x32_bf16 v[72:75], v[162:165], v[202:205], v[72:75]
	v_mfma_f32_16x16x32_bf16 v[68:71], v[170:173], v[202:205], v[68:71]
	s_setprio 0
	s_barrier
	ds_read_b128 v[174:177], v160 offset:49152
	ds_read_b128 v[178:181], v160 offset:50176
	ds_read_b128 v[182:185], v160 offset:51200
	ds_read_b128 v[186:189], v160 offset:52224
	ds_read_b128 v[190:193], v160 offset:53248
	ds_read_b128 v[194:197], v160 offset:54272
	ds_read_b128 v[198:201], v160 offset:55296
	ds_read_b128 v[202:205], v160 offset:56320
	s_add_i32 s15, s15, s45
	v_lshl_add_u64 v[206:207], v[206:207], 0, s[24:25]
	s_mov_b32 m0, s15
	global_load_lds_dwordx4 v[206:207], off
	s_add_i32 m0, s15, 0x2000
	s_add_u32 s26, s38, 0x40080
	v_lshl_add_u64 v[206:207], v[208:209], 0, s[24:25]
	s_addc_u32 s27, s39, 0
	s_add_i32 s15, s21, s45
	global_load_lds_dwordx4 v[206:207], off
	s_mov_b32 m0, s15
	v_lshl_add_u64 v[206:207], v[210:211], 0, s[24:25]
	global_load_lds_dwordx4 v148, s[26:27]
	s_add_i32 m0, s15, 0x2000
	s_nop 0
	global_load_lds_dwordx4 v152, s[26:27]
	s_mov_b32 m0, s53
	s_nop 0
	global_load_lds_dwordx4 v[206:207], off
	v_lshl_add_u64 v[206:207], v[212:213], 0, s[24:25]
	s_mov_b32 m0, s54
	s_nop 0
	global_load_lds_dwordx4 v[206:207], off
	s_waitcnt vmcnt(8)
	s_waitcnt lgkmcnt(0)
	s_barrier
	s_setprio 1
	s_waitcnt lgkmcnt(0)
	v_mfma_f32_16x16x32_bf16 v[64:67], v[132:135], v[174:177], v[64:67]
	v_mfma_f32_16x16x32_bf16 v[60:63], v[140:143], v[174:177], v[60:63]
	v_mfma_f32_16x16x32_bf16 v[48:51], v[132:135], v[182:185], v[48:51]
	v_mfma_f32_16x16x32_bf16 v[44:47], v[140:143], v[182:185], v[44:47]
	v_mfma_f32_16x16x32_bf16 v[32:35], v[132:135], v[190:193], v[32:35]
	v_mfma_f32_16x16x32_bf16 v[28:31], v[140:143], v[190:193], v[28:31]
	v_mfma_f32_16x16x32_bf16 v[16:19], v[132:135], v[198:201], v[16:19]
	v_mfma_f32_16x16x32_bf16 v[12:15], v[140:143], v[198:201], v[12:15]
	v_mfma_f32_16x16x32_bf16 v[64:67], v[136:139], v[178:181], v[64:67]
	v_mfma_f32_16x16x32_bf16 v[60:63], v[144:147], v[178:181], v[60:63]
	v_mfma_f32_16x16x32_bf16 v[48:51], v[136:139], v[186:189], v[48:51]
	v_mfma_f32_16x16x32_bf16 v[44:47], v[144:147], v[186:189], v[44:47]
	v_mfma_f32_16x16x32_bf16 v[32:35], v[136:139], v[194:197], v[32:35]
	v_mfma_f32_16x16x32_bf16 v[28:31], v[144:147], v[194:197], v[28:31]
	v_mfma_f32_16x16x32_bf16 v[16:19], v[136:139], v[202:205], v[16:19]
	v_mfma_f32_16x16x32_bf16 v[12:15], v[144:147], v[202:205], v[12:15]
	s_setprio 0
	s_setprio 1
	v_mfma_f32_16x16x32_bf16 v[56:59], v[154:157], v[174:177], v[56:59]
	v_mfma_f32_16x16x32_bf16 v[52:55], v[166:169], v[174:177], v[52:55]
	v_mfma_f32_16x16x32_bf16 v[40:43], v[154:157], v[182:185], v[40:43]
	v_mfma_f32_16x16x32_bf16 v[36:39], v[166:169], v[182:185], v[36:39]
	v_mfma_f32_16x16x32_bf16 v[24:27], v[154:157], v[190:193], v[24:27]
	v_mfma_f32_16x16x32_bf16 v[20:23], v[166:169], v[190:193], v[20:23]
	v_mfma_f32_16x16x32_bf16 v[8:11], v[154:157], v[198:201], v[8:11]
	v_mfma_f32_16x16x32_bf16 v[4:7], v[166:169], v[198:201], v[4:7]
	v_mfma_f32_16x16x32_bf16 v[56:59], v[162:165], v[178:181], v[56:59]
	v_mfma_f32_16x16x32_bf16 v[52:55], v[170:173], v[178:181], v[52:55]
	v_mfma_f32_16x16x32_bf16 v[40:43], v[162:165], v[186:189], v[40:43]
	v_mfma_f32_16x16x32_bf16 v[36:39], v[170:173], v[186:189], v[36:39]
	v_mfma_f32_16x16x32_bf16 v[24:27], v[162:165], v[194:197], v[24:27]
	v_mfma_f32_16x16x32_bf16 v[20:23], v[170:173], v[194:197], v[20:23]
	v_mfma_f32_16x16x32_bf16 v[8:11], v[162:165], v[202:205], v[8:11]
	v_mfma_f32_16x16x32_bf16 v[4:7], v[170:173], v[202:205], v[4:7]
	s_setprio 0
	s_barrier
	s_add_i32 s13, s13, 2
	s_add_u32 s30, s30, 0x100
	s_addc_u32 s31, s31, 0
	s_cmp_gt_u32 s13, 13
	s_cbranch_scc0 .LBB0_1920
	s_and_b64 vcc, exec, s[10:11]
	s_cbranch_vccz .LBB0_1923
	s_barrier

.LBB0_2007:
	v_add_u32_e32 v112, 0x10000, v239
	v_add_u32_e32 v160, 0x14000, v239
	ds_read_b128 v[100:103], v112
	ds_read_b128 v[104:107], v112 offset:1024
	ds_read_b128 v[108:111], v112 offset:2048
	ds_read_b128 v[112:115], v112 offset:3072
	ds_read_b128 v[148:151], v160
	ds_read_b128 v[152:155], v160 offset:1024
	ds_read_b128 v[156:159], v160 offset:2048
	ds_read_b128 v[160:163], v160 offset:3072
	ds_read_b128 v[164:167], v249
	ds_read_b128 v[168:171], v249 offset:1024
	ds_read_b128 v[172:175], v249 offset:2048
	ds_read_b128 v[176:179], v249 offset:3072
	ds_read_b128 v[180:183], v249 offset:4096
	ds_read_b128 v[190:193], v249 offset:5120
	ds_read_b128 v[194:197], v249 offset:6144
	ds_read_b128 v[198:201], v249 offset:7168
	s_add_u32 s3, s22, 0xfff60080
	s_addc_u32 s15, s23, -1
	s_cmp_eq_u32 s2, 36
	s_cselect_b32 s27, s16, s18
	s_cselect_b32 s3, 0, s3
	s_cselect_b32 s26, s17, s19
	s_cselect_b32 s15, 0, s15
	s_cselect_b32 s28, s0, s20
	s_cselect_b32 s33, s1, s21
	s_add_u32 s30, s27, s3
	s_addc_u32 s31, s26, s15
	s_add_i32 s34, 0, 0x10000
	s_add_i32 s35, 0, 0x14000
	s_add_i32 m0, s43, 0xc000
	s_add_u32 s26, s20, s22
	s_addc_u32 s27, s21, s23
	global_load_lds_dwordx4 v2, s[26:27]
	s_add_i32 m0, s43, 0xe000
	v_mov_b32_e32 v187, v3
	global_load_lds_dwordx4 v186, s[26:27]
	s_waitcnt vmcnt(8)
	s_waitcnt lgkmcnt(0)
	s_barrier
	s_setprio 1
	s_waitcnt lgkmcnt(0)
	v_mfma_f32_16x16x32_bf16 v[144:147], v[100:103], v[164:167], v[144:147]
	v_mfma_f32_16x16x32_bf16 v[140:143], v[108:111], v[164:167], v[140:143]
	v_mfma_f32_16x16x32_bf16 v[136:139], v[100:103], v[172:175], v[136:139]
	v_mfma_f32_16x16x32_bf16 v[132:135], v[108:111], v[172:175], v[132:135]
	v_mfma_f32_16x16x32_bf16 v[128:131], v[100:103], v[180:183], v[128:131]
	v_mfma_f32_16x16x32_bf16 v[124:127], v[108:111], v[180:183], v[124:127]
	v_mfma_f32_16x16x32_bf16 v[120:123], v[100:103], v[194:197], v[120:123]
	v_mfma_f32_16x16x32_bf16 v[116:119], v[108:111], v[194:197], v[116:119]
	v_mfma_f32_16x16x32_bf16 v[144:147], v[104:107], v[168:171], v[144:147]
	v_mfma_f32_16x16x32_bf16 v[140:143], v[112:115], v[168:171], v[140:143]
	v_mfma_f32_16x16x32_bf16 v[136:139], v[104:107], v[176:179], v[136:139]
	v_mfma_f32_16x16x32_bf16 v[132:135], v[112:115], v[176:179], v[132:135]
	v_mfma_f32_16x16x32_bf16 v[128:131], v[104:107], v[190:193], v[128:131]
	v_mfma_f32_16x16x32_bf16 v[124:127], v[112:115], v[190:193], v[124:127]
	v_mfma_f32_16x16x32_bf16 v[120:123], v[104:107], v[198:201], v[120:123]
	v_mfma_f32_16x16x32_bf16 v[116:119], v[112:115], v[198:201], v[116:119]
	s_setprio 0
	s_setprio 1
	v_mfma_f32_16x16x32_bf16 v[68:71], v[148:151], v[164:167], v[68:71]
	v_mfma_f32_16x16x32_bf16 v[60:63], v[156:159], v[164:167], v[60:63]
	v_mfma_f32_16x16x32_bf16 v[56:59], v[148:151], v[172:175], v[56:59]
	v_mfma_f32_16x16x32_bf16 v[52:55], v[156:159], v[172:175], v[52:55]
	v_mfma_f32_16x16x32_bf16 v[48:51], v[148:151], v[180:183], v[48:51]
	v_mfma_f32_16x16x32_bf16 v[44:47], v[156:159], v[180:183], v[44:47]
	v_mfma_f32_16x16x32_bf16 v[40:43], v[148:151], v[194:197], v[40:43]
	v_mfma_f32_16x16x32_bf16 v[36:39], v[156:159], v[194:197], v[36:39]
	v_mfma_f32_16x16x32_bf16 v[68:71], v[152:155], v[168:171], v[68:71]
	v_mfma_f32_16x16x32_bf16 v[60:63], v[160:163], v[168:171], v[60:63]
	v_mfma_f32_16x16x32_bf16 v[56:59], v[152:155], v[176:179], v[56:59]
	v_mfma_f32_16x16x32_bf16 v[52:55], v[160:163], v[176:179], v[52:55]
	v_mfma_f32_16x16x32_bf16 v[48:51], v[152:155], v[190:193], v[48:51]
	v_mfma_f32_16x16x32_bf16 v[44:47], v[160:163], v[190:193], v[44:47]
	v_mfma_f32_16x16x32_bf16 v[40:43], v[152:155], v[198:201], v[40:43]
	v_mfma_f32_16x16x32_bf16 v[36:39], v[160:163], v[198:201], v[36:39]
	s_setprio 0
	s_barrier
	ds_read_b128 v[164:167], v249 offset:16384
	ds_read_b128 v[168:171], v249 offset:17408
	ds_read_b128 v[172:175], v249 offset:18432
	ds_read_b128 v[176:179], v249 offset:19456
	ds_read_b128 v[180:183], v249 offset:20480
	ds_read_b128 v[190:193], v249 offset:21504
	ds_read_b128 v[194:197], v249 offset:22528
	ds_read_b128 v[198:201], v249 offset:23552
	s_add_i32 s26, s34, s42
	s_mov_b32 m0, s26
	global_load_lds_dwordx4 v184, s[30:31]
	s_add_i32 m0, s26, 0x2000
	s_add_u32 s26, s30, 0xa0000
	s_addc_u32 s27, s31, 0
	s_add_i32 s34, s35, s42
	global_load_lds_dwordx4 v188, s[30:31]
	s_mov_b32 m0, s34
	v_mov_b32_e32 v185, v3
	global_load_lds_dwordx4 v184, s[26:27]
	s_add_i32 m0, s34, 0x2000
	v_mov_b32_e32 v189, v3
	global_load_lds_dwordx4 v188, s[26:27]
	s_add_u32 s26, s28, s3
	s_addc_u32 s27, s33, s15
	s_mov_b32 m0, s43
	v_lshl_add_u64 v[202:203], s[30:31], 0, v[184:185]
	global_load_lds_dwordx4 v2, s[26:27]
	s_mov_b32 m0, s44
	v_lshl_add_u64 v[204:205], s[30:31], 0, v[188:189]
	global_load_lds_dwordx4 v186, s[26:27]
	s_waitcnt vmcnt(8)
	s_waitcnt lgkmcnt(0)
	v_lshl_add_u64 v[206:207], s[26:27], 0, v[2:3]
	v_lshl_add_u64 v[208:209], s[26:27], 0, v[186:187]
	s_barrier
	s_setprio 1
	s_waitcnt lgkmcnt(0)
	v_mfma_f32_16x16x32_bf16 v[96:99], v[100:103], v[164:167], v[96:99]
	v_mfma_f32_16x16x32_bf16 v[92:95], v[108:111], v[164:167], v[92:95]
	v_mfma_f32_16x16x32_bf16 v[88:91], v[100:103], v[172:175], v[88:91]
	v_mfma_f32_16x16x32_bf16 v[84:87], v[108:111], v[172:175], v[84:87]
	v_mfma_f32_16x16x32_bf16 v[80:83], v[100:103], v[180:183], v[80:83]
	v_mfma_f32_16x16x32_bf16 v[76:79], v[108:111], v[180:183], v[76:79]
	v_mfma_f32_16x16x32_bf16 v[72:75], v[100:103], v[194:197], v[72:75]
	v_mfma_f32_16x16x32_bf16 v[64:67], v[108:111], v[194:197], v[64:67]
	v_mfma_f32_16x16x32_bf16 v[96:99], v[104:107], v[168:171], v[96:99]
	v_mfma_f32_16x16x32_bf16 v[92:95], v[112:115], v[168:171], v[92:95]
	v_mfma_f32_16x16x32_bf16 v[88:91], v[104:107], v[176:179], v[88:91]
	v_mfma_f32_16x16x32_bf16 v[84:87], v[112:115], v[176:179], v[84:87]
	v_mfma_f32_16x16x32_bf16 v[80:83], v[104:107], v[190:193], v[80:83]
	v_mfma_f32_16x16x32_bf16 v[76:79], v[112:115], v[190:193], v[76:79]
	v_mfma_f32_16x16x32_bf16 v[72:75], v[104:107], v[198:201], v[72:75]
	v_mfma_f32_16x16x32_bf16 v[64:67], v[112:115], v[198:201], v[64:67]
	s_setprio 0
	s_setprio 1
	v_mfma_f32_16x16x32_bf16 v[32:35], v[148:151], v[164:167], v[32:35]
	v_mfma_f32_16x16x32_bf16 v[28:31], v[156:159], v[164:167], v[28:31]
	v_mfma_f32_16x16x32_bf16 v[24:27], v[148:151], v[172:175], v[24:27]
	v_mfma_f32_16x16x32_bf16 v[20:23], v[156:159], v[172:175], v[20:23]
	v_mfma_f32_16x16x32_bf16 v[16:19], v[148:151], v[180:183], v[16:19]
	v_mfma_f32_16x16x32_bf16 v[12:15], v[156:159], v[180:183], v[12:15]
	v_mfma_f32_16x16x32_bf16 v[8:11], v[148:151], v[194:197], v[8:11]
	v_mfma_f32_16x16x32_bf16 v[4:7], v[156:159], v[194:197], v[4:7]
	v_mfma_f32_16x16x32_bf16 v[32:35], v[152:155], v[168:171], v[32:35]
	v_mfma_f32_16x16x32_bf16 v[28:31], v[160:163], v[168:171], v[28:31]
	v_mfma_f32_16x16x32_bf16 v[24:27], v[152:155], v[176:179], v[24:27]
	v_mfma_f32_16x16x32_bf16 v[20:23], v[160:163], v[176:179], v[20:23]
	v_mfma_f32_16x16x32_bf16 v[16:19], v[152:155], v[190:193], v[16:19]
	v_mfma_f32_16x16x32_bf16 v[12:15], v[160:163], v[190:193], v[12:15]
	v_mfma_f32_16x16x32_bf16 v[8:11], v[152:155], v[198:201], v[8:11]
	v_mfma_f32_16x16x32_bf16 v[4:7], v[160:163], v[198:201], v[4:7]
	s_setprio 0
	s_barrier
	v_add_u32_e32 v112, 0x18000, v239
	v_add_u32_e32 v160, 0x1c000, v239
	ds_read_b128 v[100:103], v112
	ds_read_b128 v[104:107], v112 offset:1024
	ds_read_b128 v[108:111], v112 offset:2048
	ds_read_b128 v[112:115], v112 offset:3072
	ds_read_b128 v[148:151], v160
	ds_read_b128 v[152:155], v160 offset:1024
	ds_read_b128 v[156:159], v160 offset:2048
	ds_read_b128 v[160:163], v160 offset:3072
	ds_read_b128 v[164:167], v249 offset:32768
	ds_read_b128 v[168:171], v249 offset:33792
	ds_read_b128 v[172:175], v249 offset:34816
	ds_read_b128 v[176:179], v249 offset:35840
	ds_read_b128 v[180:183], v249 offset:36864
	ds_read_b128 v[190:193], v249 offset:37888
	ds_read_b128 v[194:197], v249 offset:38912
	ds_read_b128 v[198:201], v249 offset:39936
	s_add_i32 s3, 0, 0x18000
	s_add_i32 s15, 0, 0x1c000
	s_add_u32 s26, s26, 0xa0000
	s_addc_u32 s27, s27, 0
	s_mov_b32 m0, s45
	global_load_lds_dwordx4 v2, s[26:27]
	s_mov_b32 m0, s48
	s_nop 0
	global_load_lds_dwordx4 v186, s[26:27]
	s_waitcnt vmcnt(8)
	s_waitcnt lgkmcnt(0)
	s_barrier
	s_setprio 1
	s_waitcnt lgkmcnt(0)
	v_mfma_f32_16x16x32_bf16 v[144:147], v[100:103], v[164:167], v[144:147]
	v_mfma_f32_16x16x32_bf16 v[140:143], v[108:111], v[164:167], v[140:143]
	v_mfma_f32_16x16x32_bf16 v[136:139], v[100:103], v[172:175], v[136:139]
	v_mfma_f32_16x16x32_bf16 v[132:135], v[108:111], v[172:175], v[132:135]
	v_mfma_f32_16x16x32_bf16 v[128:131], v[100:103], v[180:183], v[128:131]
	v_mfma_f32_16x16x32_bf16 v[124:127], v[108:111], v[180:183], v[124:127]
	v_mfma_f32_16x16x32_bf16 v[120:123], v[100:103], v[194:197], v[120:123]
	v_mfma_f32_16x16x32_bf16 v[116:119], v[108:111], v[194:197], v[116:119]
	v_mfma_f32_16x16x32_bf16 v[144:147], v[104:107], v[168:171], v[144:147]
	v_mfma_f32_16x16x32_bf16 v[140:143], v[112:115], v[168:171], v[140:143]
	v_mfma_f32_16x16x32_bf16 v[136:139], v[104:107], v[176:179], v[136:139]
	v_mfma_f32_16x16x32_bf16 v[132:135], v[112:115], v[176:179], v[132:135]
	v_mfma_f32_16x16x32_bf16 v[128:131], v[104:107], v[190:193], v[128:131]
	v_mfma_f32_16x16x32_bf16 v[124:127], v[112:115], v[190:193], v[124:127]
	v_mfma_f32_16x16x32_bf16 v[120:123], v[104:107], v[198:201], v[120:123]
	v_mfma_f32_16x16x32_bf16 v[116:119], v[112:115], v[198:201], v[116:119]
	s_setprio 0
	s_setprio 1
	v_mfma_f32_16x16x32_bf16 v[68:71], v[148:151], v[164:167], v[68:71]
	v_mfma_f32_16x16x32_bf16 v[60:63], v[156:159], v[164:167], v[60:63]
	v_mfma_f32_16x16x32_bf16 v[56:59], v[148:151], v[172:175], v[56:59]
	v_mfma_f32_16x16x32_bf16 v[52:55], v[156:159], v[172:175], v[52:55]
	v_mfma_f32_16x16x32_bf16 v[48:51], v[148:151], v[180:183], v[48:51]
	v_mfma_f32_16x16x32_bf16 v[44:47], v[156:159], v[180:183], v[44:47]
	v_mfma_f32_16x16x32_bf16 v[40:43], v[148:151], v[194:197], v[40:43]
	v_mfma_f32_16x16x32_bf16 v[36:39], v[156:159], v[194:197], v[36:39]
	v_mfma_f32_16x16x32_bf16 v[68:71], v[152:155], v[168:171], v[68:71]
	v_mfma_f32_16x16x32_bf16 v[60:63], v[160:163], v[168:171], v[60:63]
	v_mfma_f32_16x16x32_bf16 v[56:59], v[152:155], v[176:179], v[56:59]
	v_mfma_f32_16x16x32_bf16 v[52:55], v[160:163], v[176:179], v[52:55]
	v_mfma_f32_16x16x32_bf16 v[48:51], v[152:155], v[190:193], v[48:51]
	v_mfma_f32_16x16x32_bf16 v[44:47], v[160:163], v[190:193], v[44:47]
	v_mfma_f32_16x16x32_bf16 v[40:43], v[152:155], v[198:201], v[40:43]
	v_mfma_f32_16x16x32_bf16 v[36:39], v[160:163], v[198:201], v[36:39]
	s_setprio 0
	s_barrier
	ds_read_b128 v[164:167], v249 offset:49152
	ds_read_b128 v[168:171], v249 offset:50176
	ds_read_b128 v[172:175], v249 offset:51200
	ds_read_b128 v[176:179], v249 offset:52224
	ds_read_b128 v[180:183], v249 offset:53248
	ds_read_b128 v[190:193], v249 offset:54272
	ds_read_b128 v[194:197], v249 offset:55296
	ds_read_b128 v[198:201], v249 offset:56320
	s_add_i32 s3, s3, s42
	v_lshl_add_u64 v[202:203], v[202:203], 0, s[24:25]
	s_mov_b32 m0, s3
	global_load_lds_dwordx4 v[202:203], off
	s_add_i32 m0, s3, 0x2000
	s_add_u32 s26, s30, 0xa0080
	v_lshl_add_u64 v[202:203], v[204:205], 0, s[24:25]
	s_addc_u32 s27, s31, 0
	s_add_i32 s3, s15, s42
	global_load_lds_dwordx4 v[202:203], off
	s_mov_b32 m0, s3
	v_lshl_add_u64 v[202:203], v[206:207], 0, s[24:25]
	global_load_lds_dwordx4 v184, s[26:27]
	s_add_i32 m0, s3, 0x2000
	s_nop 0
	global_load_lds_dwordx4 v188, s[26:27]
	s_mov_b32 m0, s50
	s_nop 0
	global_load_lds_dwordx4 v[202:203], off
	v_lshl_add_u64 v[202:203], v[208:209], 0, s[24:25]
	s_mov_b32 m0, s51
	s_nop 0
	global_load_lds_dwordx4 v[202:203], off
	s_waitcnt vmcnt(8)
	s_waitcnt lgkmcnt(0)
	s_barrier
	s_setprio 1
	s_waitcnt lgkmcnt(0)
	v_mfma_f32_16x16x32_bf16 v[96:99], v[100:103], v[164:167], v[96:99]
	v_mfma_f32_16x16x32_bf16 v[92:95], v[108:111], v[164:167], v[92:95]
	v_mfma_f32_16x16x32_bf16 v[88:91], v[100:103], v[172:175], v[88:91]
	v_mfma_f32_16x16x32_bf16 v[84:87], v[108:111], v[172:175], v[84:87]
	v_mfma_f32_16x16x32_bf16 v[80:83], v[100:103], v[180:183], v[80:83]
	v_mfma_f32_16x16x32_bf16 v[76:79], v[108:111], v[180:183], v[76:79]
	v_mfma_f32_16x16x32_bf16 v[72:75], v[100:103], v[194:197], v[72:75]
	v_mfma_f32_16x16x32_bf16 v[64:67], v[108:111], v[194:197], v[64:67]
	v_mfma_f32_16x16x32_bf16 v[96:99], v[104:107], v[168:171], v[96:99]
	v_mfma_f32_16x16x32_bf16 v[92:95], v[112:115], v[168:171], v[92:95]
	v_mfma_f32_16x16x32_bf16 v[88:91], v[104:107], v[176:179], v[88:91]
	v_mfma_f32_16x16x32_bf16 v[84:87], v[112:115], v[176:179], v[84:87]
	v_mfma_f32_16x16x32_bf16 v[80:83], v[104:107], v[190:193], v[80:83]
	v_mfma_f32_16x16x32_bf16 v[76:79], v[112:115], v[190:193], v[76:79]
	v_mfma_f32_16x16x32_bf16 v[72:75], v[104:107], v[198:201], v[72:75]
	v_mfma_f32_16x16x32_bf16 v[64:67], v[112:115], v[198:201], v[64:67]
	s_setprio 0
	s_setprio 1
	v_mfma_f32_16x16x32_bf16 v[32:35], v[148:151], v[164:167], v[32:35]
	v_mfma_f32_16x16x32_bf16 v[28:31], v[156:159], v[164:167], v[28:31]
	v_mfma_f32_16x16x32_bf16 v[24:27], v[148:151], v[172:175], v[24:27]
	v_mfma_f32_16x16x32_bf16 v[20:23], v[156:159], v[172:175], v[20:23]
	v_mfma_f32_16x16x32_bf16 v[16:19], v[148:151], v[180:183], v[16:19]
	v_mfma_f32_16x16x32_bf16 v[12:15], v[156:159], v[180:183], v[12:15]
	v_mfma_f32_16x16x32_bf16 v[8:11], v[148:151], v[194:197], v[8:11]
	v_mfma_f32_16x16x32_bf16 v[4:7], v[156:159], v[194:197], v[4:7]
	v_mfma_f32_16x16x32_bf16 v[32:35], v[152:155], v[168:171], v[32:35]
	v_mfma_f32_16x16x32_bf16 v[28:31], v[160:163], v[168:171], v[28:31]
	v_mfma_f32_16x16x32_bf16 v[24:27], v[152:155], v[176:179], v[24:27]
	v_mfma_f32_16x16x32_bf16 v[20:23], v[160:163], v[176:179], v[20:23]
	v_mfma_f32_16x16x32_bf16 v[16:19], v[152:155], v[190:193], v[16:19]
	v_mfma_f32_16x16x32_bf16 v[12:15], v[160:163], v[190:193], v[12:15]
	v_mfma_f32_16x16x32_bf16 v[8:11], v[152:155], v[198:201], v[8:11]
	v_mfma_f32_16x16x32_bf16 v[4:7], v[160:163], v[198:201], v[4:7]
	s_setprio 0
	s_barrier
	s_add_i32 s2, s2, 2
	s_add_u32 s22, s22, 0x100
	s_addc_u32 s23, s23, 0
	s_cmp_gt_u32 s2, 37
	s_cbranch_scc0 .LBB0_2007
	s_and_b64 vcc, exec, s[12:13]
	s_cbranch_vccz .LBB0_2010
	s_barrier
